# gathers: late u-row block combined with the later priority drop
# baseline (speedup 1.0000x reference)
.LBB0_763:
	s_cmpk_ge_i32 s58, 0x70
	s_cselect_b64 s[12:13], -1, 0
	ds_bpermute_b32 v84, v93, v92
	s_and_b64 vcc, s[12:13], s[48:49]
	v_cndmask_b32_e32 v104, v0, v94, vcc
	v_ashrrev_i32_e32 v105, 31, v104
	s_add_i32 s12, s58, 16
	s_and_b32 s12, s12, 0x70
	v_lshlrev_b64 v[104:105], 9, v[104:105]
	v_lshl_add_u64 v[104:105], s[94:95], 0, v[104:105]
	s_lshl_b32 s36, s12, 2
	s_waitcnt lgkmcnt(0)
	s_waitcnt vmcnt(32)
	v_mov_b32_e32 v92, v122
	v_ashrrev_i32_e32 v85, 31, v84
	v_lshl_add_u64 v[104:105], v[104:105], 0, s[36:37]
	v_lshl_add_u64 v[84:85], v[84:85], 3, s[8:9]
	v_lshl_add_u64 v[104:105], v[104:105], 0, v[144:145]
	global_load_dwordx2 v[84:85], v[84:85], off
	s_nop 0
	global_load_dword v86, v[72:73], off
	global_load_dword v122, v[104:105], off
	s_waitcnt vmcnt(19)
	v_dot8_i32_i4 v87, v8, v1, 0
	v_dot8_i32_i4 v104, v8, v88, 0
	v_dot8_i32_i4 v87, v9, v89, v87
	v_dot8_i32_i4 v104, v9, v90, v104
	s_waitcnt vmcnt(19)
	v_dot8_i32_i4 v9, v10, v88, 0
	v_dot8_i32_i4 v9, v11, v90, v9
	v_lshl_add_u32 v87, v87, 4, v104
	v_dot8_i32_i4 v8, v10, v1, 0
	v_dot8_i32_i4 v8, v11, v89, v8
	s_add_i32 s58, s58, 16
	v_lshl_add_u64 v[72:73], v[72:73], 0, 64
	s_nop 0
	v_lshl_add_u32 v104, v8, 4, v9
	v_dot8_i32_i4 v8, v12, v1, 0
	v_dot8_i32_i4 v9, v12, v88, 0
	v_dot8_i32_i4 v8, v13, v89, v8
	v_dot8_i32_i4 v9, v13, v90, v9
	v_readlane_b32 s12, v92, 0
	v_readlane_b32 s28, v92, 8
	v_readlane_b32 s30, v92, 9
	v_lshl_add_u32 v105, v8, 4, v9
	v_dot8_i32_i4 v8, v14, v1, 0
	v_dot8_i32_i4 v9, v14, v88, 0
	v_dot8_i32_i4 v8, v15, v89, v8
	v_dot8_i32_i4 v9, v15, v90, v9
	s_ashr_i32 s13, s12, 31
	v_readlane_b32 s14, v92, 1
	s_ashr_i32 s29, s28, 31
	v_lshl_add_u32 v106, v8, 4, v9
	v_dot8_i32_i4 v8, v16, v1, 0
	v_dot8_i32_i4 v9, v16, v88, 0
	v_dot8_i32_i4 v8, v17, v89, v8
	v_dot8_i32_i4 v9, v17, v90, v9
	s_ashr_i32 s31, s30, 31
	v_readlane_b32 s34, v92, 10
	s_lshl_b64 s[12:13], s[12:13], 9
	v_lshl_add_u32 v107, v8, 4, v9
	v_dot8_i32_i4 v8, v18, v1, 0
	v_dot8_i32_i4 v9, v18, v88, 0
	v_dot8_i32_i4 v8, v19, v89, v8
	v_dot8_i32_i4 v9, v19, v90, v9
	s_ashr_i32 s15, s14, 31
	v_readlane_b32 s16, v92, 2
	s_lshl_b64 s[28:29], s[28:29], 9
	v_lshl_add_u32 v108, v8, 4, v9
	v_dot8_i32_i4 v8, v20, v1, 0
	v_dot8_i32_i4 v9, v20, v88, 0
	v_dot8_i32_i4 v8, v21, v89, v8
	v_dot8_i32_i4 v9, v21, v90, v9
	s_lshl_b64 s[30:31], s[30:31], 9
	s_ashr_i32 s35, s34, 31
	v_readlane_b32 s38, v92, 11
	v_lshl_add_u32 v109, v8, 4, v9
	v_dot8_i32_i4 v8, v22, v1, 0
	v_dot8_i32_i4 v9, v22, v88, 0
	v_dot8_i32_i4 v8, v23, v89, v8
	v_dot8_i32_i4 v9, v23, v90, v9
	s_lshl_b64 s[14:15], s[14:15], 9
	s_ashr_i32 s17, s16, 31
	v_readlane_b32 s18, v92, 3
	v_lshl_add_u32 v110, v8, 4, v9
	v_dot8_i32_i4 v8, v24, v1, 0
	v_dot8_i32_i4 v9, v24, v88, 0
	v_dot8_i32_i4 v8, v25, v89, v8
	v_dot8_i32_i4 v9, v25, v90, v9
	s_lshl_b64 s[34:35], s[34:35], 9
	s_ashr_i32 s39, s38, 31
	s_nop 0
	v_lshl_add_u32 v111, v8, 4, v9
	v_dot8_i32_i4 v8, v38, v1, 0
	v_dot8_i32_i4 v9, v38, v88, 0
	v_dot8_i32_i4 v8, v39, v89, v8
	v_dot8_i32_i4 v9, v39, v90, v9
	s_setprio 2
	v_permlane32_swap_b32 v87, v111
	s_nop 1
	v_lshl_add_u32 v112, v8, 4, v9
	v_dot8_i32_i4 v8, v50, v1, 0
	v_dot8_i32_i4 v9, v50, v88, 0
	v_dot8_i32_i4 v8, v51, v89, v8
	v_dot8_i32_i4 v9, v51, v90, v9
	s_waitcnt lgkmcnt(0)
	v_add_u32_e32 v87, v87, v111
	v_permlane32_swap_b32 v104, v112
	v_lshl_add_u32 v113, v8, 4, v9
	v_dot8_i32_i4 v8, v48, v1, 0
	v_dot8_i32_i4 v9, v48, v88, 0
	v_dot8_i32_i4 v8, v49, v89, v8
	v_dot8_i32_i4 v9, v49, v90, v9
	s_waitcnt lgkmcnt(0)
	v_add_u32_e32 v104, v104, v112
	v_permlane32_swap_b32 v105, v113
	v_lshl_add_u32 v114, v8, 4, v9
	v_dot8_i32_i4 v8, v46, v1, 0
	v_dot8_i32_i4 v9, v46, v88, 0
	v_dot8_i32_i4 v8, v47, v89, v8
	v_dot8_i32_i4 v9, v47, v90, v9
	s_waitcnt lgkmcnt(0)
	v_add_u32_e32 v105, v105, v113
	v_permlane32_swap_b32 v106, v114
	v_lshl_add_u32 v115, v8, 4, v9
	v_dot8_i32_i4 v8, v44, v1, 0
	v_dot8_i32_i4 v9, v44, v88, 0
	v_dot8_i32_i4 v8, v45, v89, v8
	v_dot8_i32_i4 v9, v45, v90, v9
	s_waitcnt lgkmcnt(0)
	v_add_u32_e32 v106, v106, v114
	v_permlane32_swap_b32 v107, v115
	v_lshl_add_u32 v116, v8, 4, v9
	v_dot8_i32_i4 v8, v42, v1, 0
	v_dot8_i32_i4 v9, v42, v88, 0
	v_dot8_i32_i4 v8, v43, v89, v8
	v_dot8_i32_i4 v9, v43, v90, v9
	s_waitcnt lgkmcnt(0)
	v_add_u32_e32 v107, v107, v115
	v_permlane32_swap_b32 v108, v116
	v_lshl_add_u32 v117, v8, 4, v9
	v_dot8_i32_i4 v8, v40, v1, 0
	v_dot8_i32_i4 v9, v40, v88, 0
	v_dot8_i32_i4 v8, v41, v89, v8
	v_dot8_i32_i4 v9, v41, v90, v9
	s_waitcnt lgkmcnt(0)
	v_add_u32_e32 v108, v108, v116
	v_permlane32_swap_b32 v109, v117
	v_lshl_add_u32 v118, v8, 4, v9
	s_waitcnt lgkmcnt(0)
	v_add_u32_e32 v109, v109, v117
	v_permlane32_swap_b32 v110, v118
	v_readlane_b32 s50, v92, 12
	s_lshl_b64 s[16:17], s[16:17], 9
	s_ashr_i32 s19, s18, 31
	s_waitcnt lgkmcnt(0)
	v_add_u32_e32 v110, v110, v118
	v_permlane16_swap_b32 v87, v107
	v_readlane_b32 s20, v92, 4
	s_add_u32 s66, s28, s62
	s_addc_u32 s67, s29, s63
	global_load_dwordx2 v[24:25], v121, s[66:67]
	s_add_u32 s66, s30, s62
	s_addc_u32 s67, s31, s63
	global_load_dwordx2 v[38:39], v121, s[66:67]
	s_waitcnt lgkmcnt(0)
	v_add_u32_e32 v87, v87, v107
	v_permlane16_swap_b32 v104, v108
	s_lshl_b64 s[38:39], s[38:39], 9
	s_ashr_i32 s51, s50, 31
	v_readlane_b32 s52, v92, 13
	s_waitcnt lgkmcnt(0)
	v_add_u32_e32 v104, v104, v108
	v_permlane16_swap_b32 v105, v109
	s_lshl_b64 s[18:19], s[18:19], 9
	s_ashr_i32 s21, s20, 31
	v_readlane_b32 s22, v92, 5
	s_waitcnt lgkmcnt(0)
	v_add_u32_e32 v105, v105, v109
	v_permlane16_swap_b32 v106, v110
	s_add_u32 s66, s34, s62
	s_addc_u32 s67, s35, s63
	global_load_dwordx2 v[50:51], v121, s[66:67]
	s_lshl_b64 s[50:51], s[50:51], 9
	s_ashr_i32 s53, s52, 31
	s_waitcnt lgkmcnt(0)
	v_add_u32_e32 v106, v106, v110
	v_cndmask_b32_e64 v107, v87, v105, s[44:45]
	v_cndmask_b32_e64 v87, v105, v87, s[44:45]
	s_nop 0
	v_readlane_b32 s54, v92, 14
	s_lshl_b64 s[20:21], s[20:21], 9
	s_ashr_i32 s23, s22, 31
	v_readlane_b32 s24, v92, 6
	s_waitcnt lgkmcnt(0)
	v_add_u32_dpp v87, v107, v87 row_ror:8 row_mask:0xf bank_mask:0xf
	v_cndmask_b32_e64 v105, v104, v106, s[44:45]
	s_nop 1
	v_cndmask_b32_e64 v104, v106, v104, s[44:45]
	s_lshl_b64 s[52:53], s[52:53], 9
	s_ashr_i32 s55, s54, 31
	v_readlane_b32 s56, v92, 15
	s_waitcnt lgkmcnt(0)
	v_add_u32_dpp v104, v105, v104 row_ror:8 row_mask:0xf bank_mask:0xf
	v_cndmask_b32_e64 v105, v87, v104, s[46:47]
	v_cndmask_b32_e64 v87, v104, v87, s[46:47]
	s_nop 0
	v_mov_b32_dpp v104, v105 row_half_mirror row_mask:0xf bank_mask:0xf
	s_nop 1
	s_lshl_b64 s[22:23], s[22:23], 9
	s_ashr_i32 s25, s24, 31
	v_readlane_b32 s26, v92, 7
	s_lshl_b64 s[54:55], s[54:55], 9
	s_waitcnt lgkmcnt(0)
	v_add_u32_dpp v87, v104, v87 quad_perm:[3,2,1,0] row_mask:0xf bank_mask:0xf
	s_nop 1
	s_ashr_i32 s57, s56, 31
	s_lshl_b64 s[24:25], s[24:25], 9
	s_ashr_i32 s27, s26, 31
	s_lshl_b64 s[56:57], s[56:57], 9
	s_waitcnt lgkmcnt(0)
	v_add_u32_dpp v87, v87, v87 quad_perm:[2,3,0,1] row_mask:0xf bank_mask:0xf
	s_nop 1
	s_lshl_b64 s[26:27], s[26:27], 9
	s_waitcnt lgkmcnt(0)
	v_add_u32_dpp v87, v87, v87 quad_perm:[1,0,3,2] row_mask:0xf bank_mask:0xf
	s_waitcnt vmcnt(4)
	v_mul_f32_e32 v85, v91, v85
	v_cvt_f32_i32_e32 v87, v87
	v_add_f32_e32 v87, v95, v87
	v_mul_f32_e32 v85, v85, v87
	v_mul_f32_e32 v87, 0x3d372713, v85
	v_mul_f32_e32 v87, v85, v87
	v_fma_f32 v87, v85, v87, v85
	v_mul_f32_e32 v87, 0x3fcc422a, v87
	v_mul_f32_e32 v87, 0xbfb8aa3b, v87
	v_exp_f32_e32 v87, v87
	s_nop 0
	v_add_f32_e32 v87, 1.0, v87
	v_rcp_f32_e32 v87, v87
	s_nop 0
	v_pk_mul_f32 v[84:85], v[84:85], v[86:87]
	s_waitcnt vmcnt(21)
	v_alignbit_b32 v224, v82, v82, 4
	v_pk_mul_f32 v[84:85], v[84:85], v[84:85] op_sel:[0,1] op_sel_hi:[1,0]
	v_cvt_f16_f32_e32 v120, v84
	s_add_u32 s66, s38, s62
	s_addc_u32 s67, s39, s63
	global_load_dwordx2 v[48:49], v121, s[66:67]
	s_add_u32 s66, s50, s62
	s_addc_u32 s67, s51, s63
	global_load_dwordx2 v[46:47], v121, s[66:67]
	s_add_u32 s66, s52, s62
	s_addc_u32 s67, s53, s63
	global_load_dwordx2 v[44:45], v121, s[66:67]
	s_add_u32 s66, s54, s62
	s_addc_u32 s67, s55, s63
	global_load_dwordx2 v[42:43], v121, s[66:67]
	s_add_u32 s66, s56, s62
	s_addc_u32 s67, s57, s63
	global_load_dwordx2 v[40:41], v121, s[66:67]
	s_add_u32 s66, s12, s62
	s_addc_u32 s67, s13, s63
	global_load_dwordx2 v[8:9], v121, s[66:67]
	s_add_u32 s66, s14, s62
	s_addc_u32 s67, s15, s63
	global_load_dwordx2 v[10:11], v121, s[66:67]
	s_add_u32 s66, s16, s62
	s_addc_u32 s67, s17, s63
	global_load_dwordx2 v[12:13], v121, s[66:67]
	s_add_u32 s66, s18, s62
	s_addc_u32 s67, s19, s63
	global_load_dwordx2 v[14:15], v121, s[66:67]
	s_add_u32 s66, s20, s62
	s_addc_u32 s67, s21, s63
	global_load_dwordx2 v[16:17], v121, s[66:67]
	s_add_u32 s66, s22, s62
	s_addc_u32 s67, s23, s63
	global_load_dwordx2 v[18:19], v121, s[66:67]
	s_add_u32 s66, s24, s62
	s_addc_u32 s67, s25, s63
	global_load_dwordx2 v[20:21], v121, s[66:67]
	s_add_u32 s66, s26, s62
	s_addc_u32 s67, s27, s63
	global_load_dwordx2 v[22:23], v121, s[66:67]
	v_and_b32_e32 v86, 0x7070707, v82
	v_readlane_b32 s36, v120, 0
	v_and_b32_e32 v87, 0x7070707, v224
	v_perm_b32 v86, s2, v205, v86
	v_perm_b32 v87, s2, v205, v87
	v_and_or_b32 v86, v82, s4, v86
	v_and_or_b32 v82, v224, s4, v87
	v_perm_b32 v87, v82, v86, s5
	v_perm_b32 v104, v82, v86, s33
	v_perm_b32 v105, v82, v86, s0
	v_perm_b32 v82, v82, v86, s1
	v_pk_fma_f16 v86, v87, s36, v103 op_sel_hi:[1,0,1]
	v_pk_fma_f16 v87, v104, s36, v102 op_sel_hi:[1,0,1]
	v_alignbit_b32 v225, v83, v83, 4
	v_pk_fma_f16 v82, v82, s36, v100 op_sel_hi:[1,0,1]
	v_and_b32_e32 v100, 0x7070707, v83
	v_and_b32_e32 v102, 0x7070707, v225
	v_perm_b32 v100, s2, v205, v100
	v_perm_b32 v102, s2, v205, v102
	v_and_or_b32 v100, v83, s4, v100
	v_and_or_b32 v83, v225, s4, v102
	v_perm_b32 v102, v83, v100, s5
	v_perm_b32 v103, v83, v100, s33
	v_perm_b32 v104, v83, v100, s0
	v_perm_b32 v83, v83, v100, s1
	v_readlane_b32 s59, v120, 4
	s_waitcnt vmcnt(33)
	v_alignbit_b32 v224, v80, v80, 4
	v_pk_fma_f16 v101, v105, s36, v101 op_sel_hi:[1,0,1]
	v_pk_fma_f16 v99, v102, s36, v99 op_sel_hi:[1,0,1]
	v_pk_fma_f16 v98, v103, s36, v98 op_sel_hi:[1,0,1]
	v_pk_fma_f16 v97, v104, s36, v97 op_sel_hi:[1,0,1]
	v_pk_fma_f16 v83, v83, s36, v96 op_sel_hi:[1,0,1]
	s_setprio 0
	v_and_b32_e32 v96, 0x7070707, v80
	v_and_b32_e32 v100, 0x7070707, v224
	v_perm_b32 v96, s2, v205, v96
	v_perm_b32 v100, s2, v205, v100
	v_and_or_b32 v96, v80, s4, v96
	v_and_or_b32 v80, v224, s4, v100
	v_perm_b32 v100, v80, v96, s5
	v_perm_b32 v102, v80, v96, s33
	v_perm_b32 v103, v80, v96, s0
	v_perm_b32 v80, v80, v96, s1
	v_pk_fma_f16 v86, v100, s59, v86 op_sel_hi:[1,0,1]
	v_alignbit_b32 v225, v81, v81, 4
	v_pk_fma_f16 v80, v80, s59, v82 op_sel_hi:[1,0,1]
	v_and_b32_e32 v82, 0x7070707, v81
	v_and_b32_e32 v100, 0x7070707, v225
	v_pk_fma_f16 v96, v103, s59, v101 op_sel_hi:[1,0,1]
	v_perm_b32 v82, s2, v205, v82
	v_perm_b32 v100, s2, v205, v100
	v_and_or_b32 v82, v81, s4, v82
	v_and_or_b32 v81, v225, s4, v100
	v_perm_b32 v100, v81, v82, s5
	v_pk_fma_f16 v87, v102, s59, v87 op_sel_hi:[1,0,1]
	v_perm_b32 v101, v81, v82, s33
	v_perm_b32 v102, v81, v82, s0
	v_perm_b32 v81, v81, v82, s1
	v_pk_fma_f16 v82, v100, s59, v99 op_sel_hi:[1,0,1]
	v_readlane_b32 s60, v120, 8
	s_waitcnt vmcnt(32)
	v_alignbit_b32 v224, v78, v78, 4
	v_pk_fma_f16 v98, v101, s59, v98 op_sel_hi:[1,0,1]
	v_pk_fma_f16 v97, v102, s59, v97 op_sel_hi:[1,0,1]
	v_pk_fma_f16 v81, v81, s59, v83 op_sel_hi:[1,0,1]
	v_and_b32_e32 v85, 0x7070707, v78
	v_and_b32_e32 v99, 0x7070707, v224
	v_perm_b32 v85, s2, v205, v85
	v_perm_b32 v99, s2, v205, v99
	v_and_or_b32 v85, v78, s4, v85
	v_and_or_b32 v78, v224, s4, v99
	v_perm_b32 v99, v78, v85, s5
	v_perm_b32 v100, v78, v85, s33
	v_perm_b32 v101, v78, v85, s0
	v_perm_b32 v78, v78, v85, s1
	v_pk_fma_f16 v85, v99, s60, v86 op_sel_hi:[1,0,1]
	v_pk_fma_f16 v86, v100, s60, v87 op_sel_hi:[1,0,1]
	v_pk_fma_f16 v87, v101, s60, v96 op_sel_hi:[1,0,1]
	v_alignbit_b32 v225, v79, v79, 4
	v_pk_fma_f16 v78, v78, s60, v80 op_sel_hi:[1,0,1]
	v_and_b32_e32 v80, 0x7070707, v79
	v_and_b32_e32 v96, 0x7070707, v225
	v_perm_b32 v80, s2, v205, v80
	v_perm_b32 v96, s2, v205, v96
	v_and_or_b32 v80, v79, s4, v80
	v_and_or_b32 v79, v225, s4, v96
	v_perm_b32 v96, v79, v80, s5
	v_perm_b32 v100, v79, v80, s0
	v_perm_b32 v99, v79, v80, s33
	v_perm_b32 v79, v79, v80, s1
	v_pk_fma_f16 v80, v96, s60, v82 op_sel_hi:[1,0,1]
	v_pk_fma_f16 v96, v100, s60, v97 op_sel_hi:[1,0,1]
	v_readlane_b32 s36, v120, 12
	s_waitcnt vmcnt(31)
	v_alignbit_b32 v224, v76, v76, 4
	v_pk_fma_f16 v82, v99, s60, v98 op_sel_hi:[1,0,1]
	v_pk_fma_f16 v79, v79, s60, v81 op_sel_hi:[1,0,1]
	v_and_b32_e32 v83, 0x7070707, v76
	v_and_b32_e32 v97, 0x7070707, v224
	v_perm_b32 v83, s2, v205, v83
	v_perm_b32 v97, s2, v205, v97
	v_and_or_b32 v83, v76, s4, v83
	v_and_or_b32 v76, v224, s4, v97
	v_perm_b32 v97, v76, v83, s5
	v_perm_b32 v98, v76, v83, s33
	v_perm_b32 v99, v76, v83, s0
	v_perm_b32 v76, v76, v83, s1
	v_pk_fma_f16 v83, v97, s36, v85 op_sel_hi:[1,0,1]
	v_pk_fma_f16 v85, v98, s36, v86 op_sel_hi:[1,0,1]
	v_pk_fma_f16 v86, v99, s36, v87 op_sel_hi:[1,0,1]
	v_alignbit_b32 v225, v77, v77, 4
	v_pk_fma_f16 v76, v76, s36, v78 op_sel_hi:[1,0,1]
	v_and_b32_e32 v78, 0x7070707, v77
	v_and_b32_e32 v87, 0x7070707, v225
	v_perm_b32 v78, s2, v205, v78
	v_perm_b32 v87, s2, v205, v87
	v_and_or_b32 v78, v77, s4, v78
	v_and_or_b32 v77, v225, s4, v87
	v_perm_b32 v87, v77, v78, s5
	v_perm_b32 v97, v77, v78, s33
	v_perm_b32 v98, v77, v78, s0
	v_perm_b32 v77, v77, v78, s1
	v_pk_fma_f16 v78, v87, s36, v80 op_sel_hi:[1,0,1]
	v_readlane_b32 s59, v120, 16
	s_waitcnt vmcnt(30)
	v_alignbit_b32 v224, v74, v74, 4
	v_pk_fma_f16 v80, v97, s36, v82 op_sel_hi:[1,0,1]
	v_pk_fma_f16 v82, v98, s36, v96 op_sel_hi:[1,0,1]
	v_pk_fma_f16 v77, v77, s36, v79 op_sel_hi:[1,0,1]
	v_and_b32_e32 v81, 0x7070707, v74
	v_and_b32_e32 v87, 0x7070707, v224
	v_perm_b32 v81, s2, v205, v81
	v_perm_b32 v87, s2, v205, v87
	v_and_or_b32 v81, v74, s4, v81
	v_and_or_b32 v74, v224, s4, v87
	v_perm_b32 v87, v74, v81, s5
	v_perm_b32 v96, v74, v81, s33
	v_perm_b32 v97, v74, v81, s0
	v_perm_b32 v74, v74, v81, s1
	v_pk_fma_f16 v81, v87, s59, v83 op_sel_hi:[1,0,1]
	v_pk_fma_f16 v83, v96, s59, v85 op_sel_hi:[1,0,1]
	v_pk_fma_f16 v85, v97, s59, v86 op_sel_hi:[1,0,1]
	v_alignbit_b32 v225, v75, v75, 4
	v_pk_fma_f16 v74, v74, s59, v76 op_sel_hi:[1,0,1]
	v_and_b32_e32 v76, 0x7070707, v75
	v_and_b32_e32 v86, 0x7070707, v225
	v_perm_b32 v76, s2, v205, v76
	v_perm_b32 v86, s2, v205, v86
	v_and_or_b32 v76, v75, s4, v76
	v_and_or_b32 v75, v225, s4, v86
	v_perm_b32 v86, v75, v76, s5
	v_perm_b32 v87, v75, v76, s33
	v_perm_b32 v96, v75, v76, s0
	v_perm_b32 v75, v75, v76, s1
	v_pk_fma_f16 v76, v86, s59, v78 op_sel_hi:[1,0,1]
	v_pk_fma_f16 v78, v87, s59, v80 op_sel_hi:[1,0,1]
	v_pk_fma_f16 v80, v96, s59, v82 op_sel_hi:[1,0,1]
	v_readlane_b32 s60, v120, 20
	s_waitcnt vmcnt(29)
	v_alignbit_b32 v224, v70, v70, 4
	v_pk_fma_f16 v75, v75, s59, v77 op_sel_hi:[1,0,1]
	v_and_b32_e32 v79, 0x7070707, v70
	v_and_b32_e32 v82, 0x7070707, v224
	v_perm_b32 v79, s2, v205, v79
	v_perm_b32 v82, s2, v205, v82
	v_and_or_b32 v79, v70, s4, v79
	v_and_or_b32 v70, v224, s4, v82
	v_perm_b32 v82, v70, v79, s5
	v_perm_b32 v86, v70, v79, s33
	v_perm_b32 v87, v70, v79, s0
	v_perm_b32 v70, v70, v79, s1
	v_pk_fma_f16 v79, v82, s60, v81 op_sel_hi:[1,0,1]
	v_pk_fma_f16 v81, v86, s60, v83 op_sel_hi:[1,0,1]
	v_alignbit_b32 v225, v71, v71, 4
	v_pk_fma_f16 v70, v70, s60, v74 op_sel_hi:[1,0,1]
	v_and_b32_e32 v74, 0x7070707, v71
	v_and_b32_e32 v83, 0x7070707, v225
	v_pk_fma_f16 v82, v87, s60, v85 op_sel_hi:[1,0,1]
	v_perm_b32 v74, s2, v205, v74
	v_perm_b32 v83, s2, v205, v83
	v_and_or_b32 v74, v71, s4, v74
	v_and_or_b32 v71, v225, s4, v83
	v_perm_b32 v83, v71, v74, s5
	v_perm_b32 v85, v71, v74, s33
	v_perm_b32 v86, v71, v74, s0
	v_perm_b32 v71, v71, v74, s1
	v_pk_fma_f16 v74, v83, s60, v76 op_sel_hi:[1,0,1]
	v_pk_fma_f16 v76, v85, s60, v78 op_sel_hi:[1,0,1]
	v_pk_fma_f16 v78, v86, s60, v80 op_sel_hi:[1,0,1]
	v_readlane_b32 s36, v120, 24
	s_waitcnt vmcnt(28)
	v_alignbit_b32 v224, v68, v68, 4
	v_pk_fma_f16 v71, v71, s60, v75 op_sel_hi:[1,0,1]
	v_and_b32_e32 v77, 0x7070707, v68
	v_and_b32_e32 v80, 0x7070707, v224
	v_perm_b32 v77, s2, v205, v77
	v_perm_b32 v80, s2, v205, v80
	v_and_or_b32 v77, v68, s4, v77
	v_and_or_b32 v68, v224, s4, v80
	v_perm_b32 v80, v68, v77, s5
	v_perm_b32 v83, v68, v77, s33
	v_perm_b32 v85, v68, v77, s0
	v_perm_b32 v68, v68, v77, s1
	v_pk_fma_f16 v77, v80, s36, v79 op_sel_hi:[1,0,1]
	v_pk_fma_f16 v79, v83, s36, v81 op_sel_hi:[1,0,1]
	v_alignbit_b32 v225, v69, v69, 4
	v_pk_fma_f16 v68, v68, s36, v70 op_sel_hi:[1,0,1]
	v_and_b32_e32 v70, 0x7070707, v69
	v_and_b32_e32 v81, 0x7070707, v225
	v_pk_fma_f16 v80, v85, s36, v82 op_sel_hi:[1,0,1]
	v_perm_b32 v70, s2, v205, v70
	v_perm_b32 v81, s2, v205, v81
	v_and_or_b32 v70, v69, s4, v70
	v_and_or_b32 v69, v225, s4, v81
	v_perm_b32 v81, v69, v70, s5
	v_perm_b32 v82, v69, v70, s33
	v_perm_b32 v83, v69, v70, s0
	v_perm_b32 v69, v69, v70, s1
	v_pk_fma_f16 v70, v81, s36, v74 op_sel_hi:[1,0,1]
	v_pk_fma_f16 v74, v82, s36, v76 op_sel_hi:[1,0,1]
	v_pk_fma_f16 v76, v83, s36, v78 op_sel_hi:[1,0,1]
	v_readlane_b32 s59, v120, 28
	s_waitcnt vmcnt(25)
	v_alignbit_b32 v224, v64, v64, 4
	v_pk_fma_f16 v69, v69, s36, v71 op_sel_hi:[1,0,1]
	v_and_b32_e32 v75, 0x7070707, v64
	v_and_b32_e32 v78, 0x7070707, v224
	v_perm_b32 v75, s2, v205, v75
	v_perm_b32 v78, s2, v205, v78
	v_and_or_b32 v75, v64, s4, v75
	v_and_or_b32 v64, v224, s4, v78
	v_perm_b32 v78, v64, v75, s5
	v_perm_b32 v81, v64, v75, s33
	v_perm_b32 v82, v64, v75, s0
	v_perm_b32 v64, v64, v75, s1
	v_pk_fma_f16 v75, v78, s59, v77 op_sel_hi:[1,0,1]
	v_pk_fma_f16 v77, v81, s59, v79 op_sel_hi:[1,0,1]
	v_alignbit_b32 v225, v65, v65, 4
	v_pk_fma_f16 v64, v64, s59, v68 op_sel_hi:[1,0,1]
	v_and_b32_e32 v68, 0x7070707, v65
	v_and_b32_e32 v79, 0x7070707, v225
	v_pk_fma_f16 v78, v82, s59, v80 op_sel_hi:[1,0,1]
	s_add_u32 s66, s12, s64
	s_addc_u32 s67, s13, s65
	global_load_dwordx2 v[82:83], v121, s[66:67]
	v_perm_b32 v68, s2, v205, v68
	v_perm_b32 v79, s2, v205, v79
	v_and_or_b32 v68, v65, s4, v68
	v_and_or_b32 v65, v225, s4, v79
	v_perm_b32 v79, v65, v68, s5
	v_perm_b32 v80, v65, v68, s33
	v_perm_b32 v81, v65, v68, s0
	v_perm_b32 v65, v65, v68, s1
	v_pk_fma_f16 v68, v79, s59, v70 op_sel_hi:[1,0,1]
	v_pk_fma_f16 v70, v80, s59, v74 op_sel_hi:[1,0,1]
	v_pk_fma_f16 v74, v81, s59, v76 op_sel_hi:[1,0,1]
	v_readlane_b32 s60, v120, 32
	s_waitcnt vmcnt(25)
	v_alignbit_b32 v224, v62, v62, 4
	v_pk_fma_f16 v65, v65, s59, v69 op_sel_hi:[1,0,1]
	v_and_b32_e32 v71, 0x7070707, v62
	v_and_b32_e32 v76, 0x7070707, v224
	v_perm_b32 v71, s2, v205, v71
	v_perm_b32 v76, s2, v205, v76
	v_and_or_b32 v71, v62, s4, v71
	v_and_or_b32 v62, v224, s4, v76
	v_perm_b32 v76, v62, v71, s5
	v_perm_b32 v79, v62, v71, s33
	v_perm_b32 v80, v62, v71, s0
	v_perm_b32 v62, v62, v71, s1
	v_pk_fma_f16 v71, v76, s60, v75 op_sel_hi:[1,0,1]
	v_pk_fma_f16 v75, v79, s60, v77 op_sel_hi:[1,0,1]
	v_alignbit_b32 v225, v63, v63, 4
	v_pk_fma_f16 v62, v62, s60, v64 op_sel_hi:[1,0,1]
	v_and_b32_e32 v64, 0x7070707, v63
	v_and_b32_e32 v77, 0x7070707, v225
	v_pk_fma_f16 v76, v80, s60, v78 op_sel_hi:[1,0,1]
	s_add_u32 s66, s14, s64
	s_addc_u32 s67, s15, s65
	global_load_dwordx2 v[80:81], v121, s[66:67]
	v_perm_b32 v64, s2, v205, v64
	v_perm_b32 v77, s2, v205, v77
	v_and_or_b32 v64, v63, s4, v64
	v_and_or_b32 v63, v225, s4, v77
	v_perm_b32 v77, v63, v64, s5
	v_perm_b32 v78, v63, v64, s33
	v_perm_b32 v79, v63, v64, s0
	v_perm_b32 v63, v63, v64, s1
	v_pk_fma_f16 v64, v77, s60, v68 op_sel_hi:[1,0,1]
	v_pk_fma_f16 v68, v78, s60, v70 op_sel_hi:[1,0,1]
	v_pk_fma_f16 v70, v79, s60, v74 op_sel_hi:[1,0,1]
	v_readlane_b32 s36, v120, 36
	s_waitcnt vmcnt(29)
	v_alignbit_b32 v224, v66, v66, 4
	v_pk_fma_f16 v63, v63, s60, v65 op_sel_hi:[1,0,1]
	v_and_b32_e32 v69, 0x7070707, v66
	v_and_b32_e32 v74, 0x7070707, v224
	v_perm_b32 v69, s2, v205, v69
	v_perm_b32 v74, s2, v205, v74
	v_and_or_b32 v69, v66, s4, v69
	v_and_or_b32 v66, v224, s4, v74
	v_perm_b32 v74, v66, v69, s5
	v_perm_b32 v77, v66, v69, s33
	v_perm_b32 v78, v66, v69, s0
	v_perm_b32 v66, v66, v69, s1
	v_pk_fma_f16 v69, v74, s36, v71 op_sel_hi:[1,0,1]
	v_pk_fma_f16 v71, v77, s36, v75 op_sel_hi:[1,0,1]
	v_alignbit_b32 v225, v67, v67, 4
	v_pk_fma_f16 v62, v66, s36, v62 op_sel_hi:[1,0,1]
	v_and_b32_e32 v66, 0x7070707, v67
	v_and_b32_e32 v75, 0x7070707, v225
	v_pk_fma_f16 v74, v78, s36, v76 op_sel_hi:[1,0,1]
	s_add_u32 s66, s16, s64
	s_addc_u32 s67, s17, s65
	global_load_dwordx2 v[78:79], v121, s[66:67]
	v_perm_b32 v66, s2, v205, v66
	v_perm_b32 v75, s2, v205, v75
	v_and_or_b32 v66, v67, s4, v66
	v_and_or_b32 v67, v225, s4, v75
	v_perm_b32 v76, v67, v66, s33
	v_perm_b32 v77, v67, v66, s0
	v_perm_b32 v75, v67, v66, s5
	v_perm_b32 v66, v67, v66, s1
	v_pk_fma_f16 v67, v76, s36, v68 op_sel_hi:[1,0,1]
	v_pk_fma_f16 v68, v77, s36, v70 op_sel_hi:[1,0,1]
	v_readlane_b32 s59, v120, 40
	s_waitcnt vmcnt(26)
	v_alignbit_b32 v224, v60, v60, 4
	v_pk_fma_f16 v64, v75, s36, v64 op_sel_hi:[1,0,1]
	v_pk_fma_f16 v63, v66, s36, v63 op_sel_hi:[1,0,1]
	v_and_b32_e32 v66, 0x7070707, v60
	v_and_b32_e32 v70, 0x7070707, v224
	v_perm_b32 v66, s2, v205, v66
	v_perm_b32 v70, s2, v205, v70
	v_and_or_b32 v66, v60, s4, v66
	v_and_or_b32 v60, v224, s4, v70
	v_perm_b32 v70, v60, v66, s5
	v_perm_b32 v75, v60, v66, s33
	v_perm_b32 v76, v60, v66, s0
	v_perm_b32 v60, v60, v66, s1
	v_pk_fma_f16 v66, v70, s59, v69 op_sel_hi:[1,0,1]
	v_pk_fma_f16 v69, v75, s59, v71 op_sel_hi:[1,0,1]
	v_alignbit_b32 v225, v61, v61, 4
	v_pk_fma_f16 v60, v60, s59, v62 op_sel_hi:[1,0,1]
	v_and_b32_e32 v62, 0x7070707, v61
	v_and_b32_e32 v71, 0x7070707, v225
	v_pk_fma_f16 v70, v76, s59, v74 op_sel_hi:[1,0,1]
	s_add_u32 s66, s18, s64
	s_addc_u32 s67, s19, s65
	global_load_dwordx2 v[76:77], v121, s[66:67]
	v_perm_b32 v62, s2, v205, v62
	v_perm_b32 v71, s2, v205, v71
	v_and_or_b32 v62, v61, s4, v62
	v_and_or_b32 v61, v225, s4, v71
	v_perm_b32 v71, v61, v62, s5
	v_perm_b32 v74, v61, v62, s33
	v_perm_b32 v75, v61, v62, s0
	v_perm_b32 v61, v61, v62, s1
	v_pk_fma_f16 v62, v71, s59, v64 op_sel_hi:[1,0,1]
	v_pk_fma_f16 v64, v74, s59, v67 op_sel_hi:[1,0,1]
	v_pk_fma_f16 v67, v75, s59, v68 op_sel_hi:[1,0,1]
	v_readlane_b32 s60, v120, 44
	s_waitcnt vmcnt(26)
	v_alignbit_b32 v224, v58, v58, 4
	v_pk_fma_f16 v61, v61, s59, v63 op_sel_hi:[1,0,1]
	v_and_b32_e32 v65, 0x7070707, v58
	v_and_b32_e32 v68, 0x7070707, v224
	v_perm_b32 v65, s2, v205, v65
	v_perm_b32 v68, s2, v205, v68
	v_and_or_b32 v65, v58, s4, v65
	v_and_or_b32 v58, v224, s4, v68
	v_perm_b32 v68, v58, v65, s5
	v_perm_b32 v71, v58, v65, s33
	v_perm_b32 v74, v58, v65, s0
	v_perm_b32 v58, v58, v65, s1
	v_pk_fma_f16 v65, v68, s60, v66 op_sel_hi:[1,0,1]
	v_pk_fma_f16 v66, v71, s60, v69 op_sel_hi:[1,0,1]
	v_alignbit_b32 v225, v59, v59, 4
	v_pk_fma_f16 v58, v58, s60, v60 op_sel_hi:[1,0,1]
	v_and_b32_e32 v60, 0x7070707, v59
	v_and_b32_e32 v69, 0x7070707, v225
	v_pk_fma_f16 v68, v74, s60, v70 op_sel_hi:[1,0,1]
	s_add_u32 s66, s20, s64
	s_addc_u32 s67, s21, s65
	global_load_dwordx2 v[74:75], v121, s[66:67]
	v_perm_b32 v60, s2, v205, v60
	v_perm_b32 v69, s2, v205, v69
	v_and_or_b32 v60, v59, s4, v60
	v_and_or_b32 v59, v225, s4, v69
	v_perm_b32 v69, v59, v60, s5
	v_perm_b32 v70, v59, v60, s33
	v_perm_b32 v71, v59, v60, s0
	v_perm_b32 v59, v59, v60, s1
	v_pk_fma_f16 v60, v69, s60, v62 op_sel_hi:[1,0,1]
	v_pk_fma_f16 v62, v70, s60, v64 op_sel_hi:[1,0,1]
	v_pk_fma_f16 v64, v71, s60, v67 op_sel_hi:[1,0,1]
	v_readlane_b32 s36, v120, 48
	s_waitcnt vmcnt(26)
	v_alignbit_b32 v224, v56, v56, 4
	v_pk_fma_f16 v59, v59, s60, v61 op_sel_hi:[1,0,1]
	v_and_b32_e32 v63, 0x7070707, v56
	v_and_b32_e32 v67, 0x7070707, v224
	v_perm_b32 v63, s2, v205, v63
	v_perm_b32 v67, s2, v205, v67
	v_and_or_b32 v63, v56, s4, v63
	v_and_or_b32 v56, v224, s4, v67
	v_perm_b32 v67, v56, v63, s5
	v_perm_b32 v69, v56, v63, s33
	v_perm_b32 v70, v56, v63, s0
	v_perm_b32 v56, v56, v63, s1
	v_pk_fma_f16 v63, v67, s36, v65 op_sel_hi:[1,0,1]
	v_alignbit_b32 v225, v57, v57, 4
	v_pk_fma_f16 v56, v56, s36, v58 op_sel_hi:[1,0,1]
	v_and_b32_e32 v58, 0x7070707, v57
	v_and_b32_e32 v67, 0x7070707, v225
	v_pk_fma_f16 v65, v69, s36, v66 op_sel_hi:[1,0,1]
	v_pk_fma_f16 v66, v70, s36, v68 op_sel_hi:[1,0,1]
	s_add_u32 s66, s22, s64
	s_addc_u32 s67, s23, s65
	global_load_dwordx2 v[70:71], v121, s[66:67]
	v_perm_b32 v58, s2, v205, v58
	v_perm_b32 v67, s2, v205, v67
	v_and_or_b32 v58, v57, s4, v58
	v_and_or_b32 v57, v225, s4, v67
	v_perm_b32 v67, v57, v58, s5
	v_perm_b32 v68, v57, v58, s33
	v_perm_b32 v69, v57, v58, s0
	v_perm_b32 v57, v57, v58, s1
	v_pk_fma_f16 v58, v67, s36, v60 op_sel_hi:[1,0,1]
	v_pk_fma_f16 v60, v68, s36, v62 op_sel_hi:[1,0,1]
	v_pk_fma_f16 v62, v69, s36, v64 op_sel_hi:[1,0,1]
	v_readlane_b32 s59, v120, 52
	s_waitcnt vmcnt(26)
	v_alignbit_b32 v224, v54, v54, 4
	v_pk_fma_f16 v57, v57, s36, v59 op_sel_hi:[1,0,1]
	v_and_b32_e32 v61, 0x7070707, v54
	v_and_b32_e32 v64, 0x7070707, v224
	v_perm_b32 v61, s2, v205, v61
	v_perm_b32 v64, s2, v205, v64
	v_and_or_b32 v61, v54, s4, v61
	v_and_or_b32 v54, v224, s4, v64
	v_perm_b32 v64, v54, v61, s5
	v_perm_b32 v67, v54, v61, s33
	v_perm_b32 v68, v54, v61, s0
	v_perm_b32 v54, v54, v61, s1
	v_pk_fma_f16 v61, v64, s59, v63 op_sel_hi:[1,0,1]
	v_pk_fma_f16 v63, v67, s59, v65 op_sel_hi:[1,0,1]
	v_alignbit_b32 v225, v55, v55, 4
	v_pk_fma_f16 v54, v54, s59, v56 op_sel_hi:[1,0,1]
	v_and_b32_e32 v56, 0x7070707, v55
	v_and_b32_e32 v65, 0x7070707, v225
	v_pk_fma_f16 v64, v68, s59, v66 op_sel_hi:[1,0,1]
	s_add_u32 s66, s24, s64
	s_addc_u32 s67, s25, s65
	global_load_dwordx2 v[68:69], v121, s[66:67]
	v_perm_b32 v56, s2, v205, v56
	v_perm_b32 v65, s2, v205, v65
	v_and_or_b32 v56, v55, s4, v56
	v_and_or_b32 v55, v225, s4, v65
	v_perm_b32 v65, v55, v56, s5
	v_perm_b32 v66, v55, v56, s33
	v_perm_b32 v67, v55, v56, s0
	v_perm_b32 v55, v55, v56, s1
	v_pk_fma_f16 v56, v65, s59, v58 op_sel_hi:[1,0,1]
	v_pk_fma_f16 v58, v66, s59, v60 op_sel_hi:[1,0,1]
	v_pk_fma_f16 v60, v67, s59, v62 op_sel_hi:[1,0,1]
	v_readlane_b32 s60, v120, 56
	s_waitcnt vmcnt(26)
	v_alignbit_b32 v224, v52, v52, 4
	v_pk_fma_f16 v55, v55, s59, v57 op_sel_hi:[1,0,1]
	v_and_b32_e32 v59, 0x7070707, v52
	v_and_b32_e32 v62, 0x7070707, v224
	v_perm_b32 v59, s2, v205, v59
	v_perm_b32 v62, s2, v205, v62
	v_and_or_b32 v59, v52, s4, v59
	v_and_or_b32 v52, v224, s4, v62
	v_perm_b32 v62, v52, v59, s5
	v_perm_b32 v65, v52, v59, s33
	v_perm_b32 v66, v52, v59, s0
	v_perm_b32 v52, v52, v59, s1
	v_pk_fma_f16 v59, v62, s60, v61 op_sel_hi:[1,0,1]
	v_pk_fma_f16 v61, v65, s60, v63 op_sel_hi:[1,0,1]
	v_alignbit_b32 v225, v53, v53, 4
	v_pk_fma_f16 v52, v52, s60, v54 op_sel_hi:[1,0,1]
	v_and_b32_e32 v54, 0x7070707, v53
	v_and_b32_e32 v63, 0x7070707, v225
	v_pk_fma_f16 v62, v66, s60, v64 op_sel_hi:[1,0,1]
	s_add_u32 s66, s30, s64
	s_addc_u32 s67, s31, s65
	global_load_dwordx2 v[66:67], v121, s[66:67]
	v_perm_b32 v54, s2, v205, v54
	v_perm_b32 v63, s2, v205, v63
	v_and_or_b32 v54, v53, s4, v54
	v_and_or_b32 v53, v225, s4, v63
	v_perm_b32 v63, v53, v54, s5
	v_perm_b32 v64, v53, v54, s33
	v_perm_b32 v65, v53, v54, s0
	v_perm_b32 v53, v53, v54, s1
	v_pk_fma_f16 v54, v63, s60, v56 op_sel_hi:[1,0,1]
	v_pk_fma_f16 v56, v64, s60, v58 op_sel_hi:[1,0,1]
	v_pk_fma_f16 v58, v65, s60, v60 op_sel_hi:[1,0,1]
	v_readlane_b32 s36, v120, 60
	s_waitcnt vmcnt(34)
	v_alignbit_b32 v224, v36, v36, 4
	v_pk_fma_f16 v53, v53, s60, v55 op_sel_hi:[1,0,1]
	v_and_b32_e32 v57, 0x7070707, v36
	v_and_b32_e32 v60, 0x7070707, v224
	v_perm_b32 v57, s2, v205, v57
	v_perm_b32 v60, s2, v205, v60
	v_and_or_b32 v57, v36, s4, v57
	v_and_or_b32 v36, v224, s4, v60
	v_perm_b32 v60, v36, v57, s5
	v_perm_b32 v63, v36, v57, s33
	v_perm_b32 v64, v36, v57, s0
	v_perm_b32 v36, v36, v57, s1
	v_pk_fma_f16 v100, v36, s36, v52 op_sel_hi:[1,0,1]
	v_alignbit_b32 v225, v37, v37, 4
	v_and_b32_e32 v36, 0x7070707, v37
	v_and_b32_e32 v52, 0x7070707, v225
	v_perm_b32 v36, s2, v205, v36
	v_perm_b32 v52, s2, v205, v52
	v_and_or_b32 v36, v37, s4, v36
	v_and_or_b32 v37, v225, s4, v52
	v_pk_fma_f16 v103, v60, s36, v59 op_sel_hi:[1,0,1]
	v_perm_b32 v52, v37, v36, s5
	v_perm_b32 v57, v37, v36, s33
	v_perm_b32 v59, v37, v36, s0
	v_perm_b32 v36, v37, v36, s1
	v_pk_fma_f16 v96, v36, s36, v53 op_sel_hi:[1,0,1]
	s_add_u32 s66, s56, s64
	s_addc_u32 s67, s57, s65
	global_load_dwordx2 v[36:37], v121, s[66:67]
	v_pk_fma_f16 v101, v64, s36, v62 op_sel_hi:[1,0,1]
	s_add_u32 s66, s26, s64
	s_addc_u32 s67, s27, s65
	global_load_dwordx2 v[64:65], v121, s[66:67]
	v_pk_fma_f16 v102, v63, s36, v61 op_sel_hi:[1,0,1]
	s_add_u32 s66, s28, s64
	s_addc_u32 s67, s29, s65
	global_load_dwordx2 v[62:63], v121, s[66:67]
	s_add_u32 s66, s34, s64
	s_addc_u32 s67, s35, s65
	global_load_dwordx2 v[60:61], v121, s[66:67]
	v_pk_fma_f16 v97, v59, s36, v58 op_sel_hi:[1,0,1]
	s_add_u32 s66, s38, s64
	s_addc_u32 s67, s39, s65
	global_load_dwordx2 v[58:59], v121, s[66:67]
	v_pk_fma_f16 v98, v57, s36, v56 op_sel_hi:[1,0,1]
	s_add_u32 s66, s50, s64
	s_addc_u32 s67, s51, s65
	global_load_dwordx2 v[56:57], v121, s[66:67]
	v_pk_fma_f16 v99, v52, s36, v54 op_sel_hi:[1,0,1]
	s_add_u32 s66, s52, s64
	s_addc_u32 s67, s53, s65
	global_load_dwordx2 v[54:55], v121, s[66:67]
	s_add_u32 s66, s54, s64
	s_addc_u32 s67, s55, s65
	global_load_dwordx2 v[52:53], v121, s[66:67]
	s_nop 0
	s_nop 0
	s_nop 0
	s_nop 0
	s_nop 0
	s_nop 0
	s_nop 0
	s_cmpk_eq_i32 s58, 0x90
	s_cbranch_scc0 .LBB0_763
	v_lshlrev_b64 v[0:1], 2, v[2:3]
	v_lshl_add_u64 v[2:3], v[28:29], 0, v[0:1]
	v_mov_b32_e32 v104, v208
	v_mov_b32_e32 v105, v209
	v_mov_b32_e32 v106, v210
	v_mov_b32_e32 v107, v211
	v_mov_b32_e32 v108, v212
	v_mov_b32_e32 v109, v213
	v_mov_b32_e32 v110, v214
	v_mov_b32_e32 v111, v215
	v_mov_b32_e32 v86, v216
	v_mov_b32_e32 v87, v217
	v_mov_b32_e32 v88, v218
	v_mov_b32_e32 v89, v219
	v_mov_b32_e32 v112, v220
	v_mov_b32_e32 v113, v221
	v_mov_b32_e32 v114, v222
	v_mov_b32_e32 v115, v223
	v_lshl_add_u64 v[72:73], v[32:33], 0, v[0:1]
	v_cvt_f32_f16_sdwa v1, v103 dst_sel:DWORD dst_unused:UNUSED_PAD src0_sel:WORD_1
	v_cvt_f32_f16_e32 v0, v103
	v_cvt_f32_f16_sdwa v91, v102 dst_sel:DWORD dst_unused:UNUSED_PAD src0_sel:WORD_1
	v_cvt_f32_f16_e32 v90, v102
	v_cvt_f32_f16_sdwa v103, v101 dst_sel:DWORD dst_unused:UNUSED_PAD src0_sel:WORD_1
	v_cvt_f32_f16_e32 v102, v101
	v_cvt_f32_f16_sdwa v101, v100 dst_sel:DWORD dst_unused:UNUSED_PAD src0_sel:WORD_1
	v_cvt_f32_f16_e32 v100, v100
	s_mov_b32 s18, 0x800000
	v_readlane_b32 s12, v255, 5
	v_readlane_b32 s13, v255, 6
	v_pk_add_f32 v[86:87], v[86:87], v[102:103]
	v_pk_add_f32 v[84:85], v[112:113], v[0:1]
	v_mov_b32_e32 v102, v85
	v_mov_b32_e32 v103, v87
	v_pk_add_f32 v[90:91], v[114:115], v[90:91]
	v_pk_add_f32 v[88:89], v[88:89], v[100:101]
	v_mov_b32_e32 v100, v84
	v_mov_b32_e32 v101, v86
	v_pk_mul_f32 v[102:103], v[102:103], v[102:103]
	v_mov_b32_e32 v112, v91
	v_pk_fma_f32 v[100:101], v[100:101], v[100:101], v[102:103]
	v_mov_b32_e32 v102, v90
	v_mov_b32_e32 v103, v88
	v_pk_fma_f32 v[100:101], v[102:103], v[102:103], v[100:101]
	v_cvt_f32_f16_sdwa v103, v99 dst_sel:DWORD dst_unused:UNUSED_PAD src0_sel:WORD_1
	v_cvt_f32_f16_e32 v102, v99
	v_cvt_f32_f16_sdwa v99, v98 dst_sel:DWORD dst_unused:UNUSED_PAD src0_sel:WORD_1
	v_cvt_f32_f16_e32 v98, v98
	v_mov_b32_e32 v113, v89
	v_pk_add_f32 v[102:103], v[108:109], v[102:103]
	v_cvt_f32_f16_sdwa v109, v97 dst_sel:DWORD dst_unused:UNUSED_PAD src0_sel:WORD_1
	v_cvt_f32_f16_e32 v108, v97
	v_cvt_f32_f16_sdwa v97, v96 dst_sel:DWORD dst_unused:UNUSED_PAD src0_sel:WORD_1
	v_cvt_f32_f16_e32 v96, v96
	v_pk_add_f32 v[98:99], v[110:111], v[98:99]
	v_pk_add_f32 v[104:105], v[104:105], v[108:109]
	v_mov_b32_e32 v108, v103
	v_mov_b32_e32 v109, v105
	v_pk_add_f32 v[96:97], v[106:107], v[96:97]
	v_mov_b32_e32 v106, v102
	v_mov_b32_e32 v107, v104
	v_pk_mul_f32 v[108:109], v[108:109], v[108:109]
	v_pk_fma_f32 v[100:101], v[112:113], v[112:113], v[100:101]
	v_pk_fma_f32 v[106:107], v[106:107], v[106:107], v[108:109]
	v_mov_b32_e32 v108, v98
	v_mov_b32_e32 v109, v96
	v_mov_b32_e32 v110, v99
	v_mov_b32_e32 v111, v97
	v_pk_fma_f32 v[106:107], v[108:109], v[108:109], v[106:107]
	v_add_f32_e32 v95, v100, v101
	v_pk_fma_f32 v[106:107], v[110:111], v[110:111], v[106:107]
	v_lshl_add_u64 v[34:35], v[34:35], 0, s[12:13]
	v_add_f32_e32 v95, v95, v106
	v_add_f32_e32 v95, v95, v107
	v_mov_b32_e32 v100, v95
	s_nop 1
	v_permlane32_swap_b32 v100, v95
	s_waitcnt lgkmcnt(0)
	v_add_f32_e32 v95, v95, v100
	v_mov_b32_e32 v100, v95
	s_nop 1
	v_permlane16_swap_b32 v100, v95
	s_waitcnt lgkmcnt(0)
	v_add_f32_e32 v95, v95, v100
	s_nop 1
	v_mov_b32_dpp v100, v95 row_ror:8 row_mask:0xf bank_mask:0xf
	s_waitcnt lgkmcnt(0)
	v_add_f32_e32 v95, v95, v100
	s_nop 1
	v_mov_b32_dpp v100, v95 row_half_mirror row_mask:0xf bank_mask:0xf
	s_nop 1
	v_mov_b32_dpp v100, v100 quad_perm:[3,2,1,0] row_mask:0xf bank_mask:0xf
	s_waitcnt lgkmcnt(0)
	v_add_f32_e32 v95, v95, v100
	s_nop 1
	v_mov_b32_dpp v100, v95 quad_perm:[2,3,0,1] row_mask:0xf bank_mask:0xf
	s_waitcnt lgkmcnt(0)
	v_add_f32_e32 v95, v95, v100
	s_nop 1
	v_mov_b32_dpp v100, v95 quad_perm:[1,0,3,2] row_mask:0xf bank_mask:0xf
	s_waitcnt lgkmcnt(0)
	v_add_f32_e32 v95, v95, v100
	v_fmamk_f32 v95, v95, 0x3a800000, v191
	v_cmp_gt_f32_e32 vcc, s18, v95
	v_mul_f32_e32 v100, 0x4b800000, v95
	s_nop 0
	v_cndmask_b32_e32 v95, v95, v100, vcc
	v_rsq_f32_e32 v95, v95
	s_nop 0
	v_mul_f32_e32 v100, 0x45800000, v95
	v_cndmask_b32_e32 v100, v95, v100, vcc
	v_pk_mul_f32 v[84:85], v[84:85], v[100:101] op_sel_hi:[1,0]
	v_pk_mul_f32 v[0:1], v[124:125], v[84:85]
	v_pk_mul_f32 v[84:85], v[90:91], v[100:101] op_sel_hi:[1,0]
	s_nop 0
	v_pk_mul_f32 v[2:3], v[126:127], v[84:85]
	global_store_dwordx4 v[72:73], v[0:3], off
	s_nop 1
	v_pk_mul_f32 v[84:85], v[86:87], v[100:101] op_sel_hi:[1,0]
	v_pk_mul_f32 v[0:1], v[128:129], v[84:85]
	v_pk_mul_f32 v[84:85], v[88:89], v[100:101] op_sel_hi:[1,0]
	s_nop 0
	v_pk_mul_f32 v[2:3], v[130:131], v[84:85]
	global_store_dwordx4 v[72:73], v[0:3], off offset:16
	s_nop 1
	v_pk_mul_f32 v[84:85], v[102:103], v[100:101] op_sel_hi:[1,0]
	v_pk_mul_f32 v[0:1], v[84:85], v[132:133]
	v_pk_mul_f32 v[84:85], v[98:99], v[100:101] op_sel_hi:[1,0]
	s_nop 0
	v_pk_mul_f32 v[2:3], v[84:85], v[134:135]
	global_store_dwordx4 v[72:73], v[0:3], off offset:32
	s_nop 1
	v_pk_mul_f32 v[84:85], v[104:105], v[100:101] op_sel_hi:[1,0]
	v_pk_mul_f32 v[0:1], v[84:85], v[136:137]
	v_pk_mul_f32 v[84:85], v[96:97], v[100:101] op_sel_hi:[1,0]
	s_nop 0
	v_pk_mul_f32 v[2:3], v[84:85], v[138:139]
	global_store_dwordx4 v[72:73], v[0:3], off offset:48
	s_nop 1
	v_mov_b32_e32 v0, v94
	s_andn2_b64 exec, exec, s[10:11]
	s_cbranch_execnz .LBB0_762

.LBB0_770:
	s_cmpk_ge_i32 s56, 0x70
	s_cselect_b64 s[10:11], -1, 0
	ds_bpermute_b32 v6, v97, v96
	s_and_b64 vcc, s[10:11], s[48:49]
	v_cndmask_b32_e32 v94, v0, v98, vcc
	v_ashrrev_i32_e32 v95, 31, v94
	s_add_i32 s10, s56, 16
	s_and_b32 s10, s10, 0x70
	v_lshlrev_b64 v[94:95], 9, v[94:95]
	v_lshl_add_u64 v[94:95], s[94:95], 0, v[94:95]
	s_lshl_b32 s36, s10, 2
	s_waitcnt lgkmcnt(0)
	s_waitcnt vmcnt(32)
	v_mov_b32_e32 v96, v122
	v_ashrrev_i32_e32 v7, 31, v6
	v_lshl_add_u64 v[94:95], v[94:95], 0, s[36:37]
	v_lshl_add_u64 v[6:7], v[6:7], 3, s[88:89]
	v_lshl_add_u64 v[94:95], v[94:95], 0, v[144:145]
	global_load_dwordx2 v[6:7], v[6:7], off
	s_nop 0
	global_load_dword v8, v[4:5], off
	global_load_dword v122, v[94:95], off
	s_waitcnt vmcnt(19)
	v_dot8_i32_i4 v9, v20, v1, 0
	v_dot8_i32_i4 v94, v20, v10, 0
	v_dot8_i32_i4 v9, v21, v11, v9
	v_dot8_i32_i4 v94, v21, v12, v94
	v_dot8_i32_i4 v20, v22, v1, 0
	v_dot8_i32_i4 v21, v22, v10, 0
	v_dot8_i32_i4 v20, v23, v11, v20
	v_dot8_i32_i4 v21, v23, v12, v21
	v_lshl_add_u32 v9, v9, 4, v94
	s_add_i32 s56, s56, 16
	s_nop 0
	v_lshl_add_u32 v94, v20, 4, v21
	s_waitcnt vmcnt(19)
	v_dot8_i32_i4 v20, v24, v1, 0
	v_dot8_i32_i4 v21, v24, v10, 0
	v_dot8_i32_i4 v20, v25, v11, v20
	v_dot8_i32_i4 v21, v25, v12, v21
	v_lshl_add_u64 v[4:5], v[4:5], 0, 64
	s_nop 1
	v_lshl_add_u32 v95, v20, 4, v21
	v_dot8_i32_i4 v20, v26, v1, 0
	v_dot8_i32_i4 v21, v26, v10, 0
	v_dot8_i32_i4 v20, v27, v11, v20
	v_dot8_i32_i4 v21, v27, v12, v21
	v_readlane_b32 s10, v96, 0
	s_ashr_i32 s11, s10, 31
	v_readlane_b32 s12, v96, 1
	v_lshl_add_u32 v106, v20, 4, v21
	v_dot8_i32_i4 v20, v28, v1, 0
	v_dot8_i32_i4 v21, v28, v10, 0
	v_dot8_i32_i4 v20, v29, v11, v20
	v_dot8_i32_i4 v21, v29, v12, v21
	s_lshl_b64 s[10:11], s[10:11], 9
	s_ashr_i32 s13, s12, 31
	v_readlane_b32 s14, v96, 2
	v_lshl_add_u32 v107, v20, 4, v21
	v_dot8_i32_i4 v20, v30, v1, 0
	v_dot8_i32_i4 v21, v30, v10, 0
	v_dot8_i32_i4 v20, v31, v11, v20
	v_dot8_i32_i4 v21, v31, v12, v21
	s_lshl_b64 s[12:13], s[12:13], 9
	s_ashr_i32 s15, s14, 31
	v_readlane_b32 s16, v96, 3
	v_lshl_add_u32 v108, v20, 4, v21
	v_dot8_i32_i4 v20, v32, v1, 0
	v_dot8_i32_i4 v21, v32, v10, 0
	v_dot8_i32_i4 v20, v33, v11, v20
	v_dot8_i32_i4 v21, v33, v12, v21
	s_lshl_b64 s[14:15], s[14:15], 9
	s_ashr_i32 s17, s16, 31
	s_nop 0
	v_lshl_add_u32 v109, v20, 4, v21
	v_dot8_i32_i4 v20, v34, v1, 0
	v_dot8_i32_i4 v21, v34, v10, 0
	v_dot8_i32_i4 v20, v35, v11, v20
	v_dot8_i32_i4 v21, v35, v12, v21
	v_readlane_b32 s18, v96, 4
	s_add_u32 s66, s12, s62
	s_addc_u32 s67, s13, s63
	global_load_dwordx2 v[22:23], v121, s[66:67]
	v_lshl_add_u32 v110, v20, 4, v21
	v_dot8_i32_i4 v20, v36, v1, 0
	v_dot8_i32_i4 v21, v36, v10, 0
	v_dot8_i32_i4 v20, v37, v11, v20
	v_dot8_i32_i4 v21, v37, v12, v21
	s_lshl_b64 s[16:17], s[16:17], 9
	s_ashr_i32 s19, s18, 31
	v_readlane_b32 s20, v96, 5
	v_lshl_add_u32 v111, v20, 4, v21
	v_dot8_i32_i4 v20, v38, v1, 0
	v_dot8_i32_i4 v21, v38, v10, 0
	v_dot8_i32_i4 v20, v39, v11, v20
	v_dot8_i32_i4 v21, v39, v12, v21
	s_setprio 2
	v_permlane32_swap_b32 v9, v111
	s_nop 1
	v_lshl_add_u32 v112, v20, 4, v21
	v_dot8_i32_i4 v20, v40, v1, 0
	v_dot8_i32_i4 v21, v40, v10, 0
	v_dot8_i32_i4 v20, v41, v11, v20
	v_dot8_i32_i4 v21, v41, v12, v21
	s_waitcnt lgkmcnt(0)
	v_add_u32_e32 v9, v9, v111
	v_permlane32_swap_b32 v94, v112
	v_lshl_add_u32 v113, v20, 4, v21
	v_dot8_i32_i4 v20, v60, v1, 0
	v_dot8_i32_i4 v21, v60, v10, 0
	v_dot8_i32_i4 v20, v61, v11, v20
	v_dot8_i32_i4 v21, v61, v12, v21
	s_waitcnt lgkmcnt(0)
	v_add_u32_e32 v94, v94, v112
	v_permlane32_swap_b32 v95, v113
	v_lshl_add_u32 v114, v20, 4, v21
	v_dot8_i32_i4 v20, v58, v1, 0
	v_dot8_i32_i4 v21, v58, v10, 0
	v_dot8_i32_i4 v20, v59, v11, v20
	v_dot8_i32_i4 v21, v59, v12, v21
	s_waitcnt lgkmcnt(0)
	v_add_u32_e32 v95, v95, v113
	v_permlane32_swap_b32 v106, v114
	v_lshl_add_u32 v115, v20, 4, v21
	v_dot8_i32_i4 v20, v56, v1, 0
	v_dot8_i32_i4 v21, v56, v10, 0
	v_dot8_i32_i4 v20, v57, v11, v20
	v_dot8_i32_i4 v21, v57, v12, v21
	s_waitcnt lgkmcnt(0)
	v_add_u32_e32 v106, v106, v114
	v_permlane32_swap_b32 v107, v115
	v_lshl_add_u32 v116, v20, 4, v21
	v_dot8_i32_i4 v20, v54, v1, 0
	v_dot8_i32_i4 v21, v54, v10, 0
	v_dot8_i32_i4 v20, v55, v11, v20
	v_dot8_i32_i4 v21, v55, v12, v21
	s_waitcnt lgkmcnt(0)
	v_add_u32_e32 v107, v107, v115
	v_permlane32_swap_b32 v108, v116
	v_lshl_add_u32 v117, v20, 4, v21
	v_dot8_i32_i4 v20, v52, v1, 0
	v_dot8_i32_i4 v21, v52, v10, 0
	v_dot8_i32_i4 v20, v53, v11, v20
	v_dot8_i32_i4 v21, v53, v12, v21
	s_waitcnt lgkmcnt(0)
	v_add_u32_e32 v108, v108, v116
	v_permlane32_swap_b32 v109, v117
	v_lshl_add_u32 v118, v20, 4, v21
	s_waitcnt lgkmcnt(0)
	v_add_u32_e32 v109, v109, v117
	v_permlane32_swap_b32 v110, v118
	s_add_u32 s66, s10, s62
	s_addc_u32 s67, s11, s63
	global_load_dwordx2 v[20:21], v121, s[66:67]
	s_add_u32 s66, s14, s62
	s_addc_u32 s67, s15, s63
	global_load_dwordx2 v[24:25], v121, s[66:67]
	s_waitcnt lgkmcnt(0)
	v_add_u32_e32 v110, v110, v118
	v_permlane16_swap_b32 v9, v107
	s_lshl_b64 s[18:19], s[18:19], 9
	s_ashr_i32 s21, s20, 31
	v_readlane_b32 s22, v96, 6
	s_add_u32 s66, s16, s62
	s_addc_u32 s67, s17, s63
	global_load_dwordx2 v[26:27], v121, s[66:67]
	s_waitcnt lgkmcnt(0)
	v_add_u32_e32 v9, v9, v107
	v_permlane16_swap_b32 v94, v108
	s_lshl_b64 s[20:21], s[20:21], 9
	s_ashr_i32 s23, s22, 31
	s_waitcnt lgkmcnt(0)
	v_add_u32_e32 v94, v94, v108
	v_permlane16_swap_b32 v95, v109
	v_readlane_b32 s24, v96, 7
	s_add_u32 s66, s18, s62
	s_addc_u32 s67, s19, s63
	global_load_dwordx2 v[28:29], v121, s[66:67]
	s_waitcnt lgkmcnt(0)
	v_add_u32_e32 v95, v95, v109
	v_permlane16_swap_b32 v106, v110
	s_lshl_b64 s[22:23], s[22:23], 9
	s_ashr_i32 s25, s24, 31
	v_readlane_b32 s26, v96, 8
	s_waitcnt lgkmcnt(0)
	v_add_u32_e32 v106, v106, v110
	v_cndmask_b32_e64 v107, v9, v95, s[44:45]
	v_cndmask_b32_e64 v9, v95, v9, s[44:45]
	s_nop 0
	s_add_u32 s66, s20, s62
	s_addc_u32 s67, s21, s63
	global_load_dwordx2 v[30:31], v121, s[66:67]
	s_lshl_b64 s[24:25], s[24:25], 9
	s_ashr_i32 s27, s26, 31
	s_waitcnt lgkmcnt(0)
	v_add_u32_dpp v9, v107, v9 row_ror:8 row_mask:0xf bank_mask:0xf
	v_cndmask_b32_e64 v95, v94, v106, s[44:45]
	s_nop 1
	v_cndmask_b32_e64 v94, v106, v94, s[44:45]
	v_readlane_b32 s28, v96, 9
	s_add_u32 s66, s22, s62
	s_addc_u32 s67, s23, s63
	global_load_dwordx2 v[32:33], v121, s[66:67]
	s_waitcnt lgkmcnt(0)
	v_add_u32_dpp v94, v95, v94 row_ror:8 row_mask:0xf bank_mask:0xf
	v_cndmask_b32_e64 v95, v9, v94, s[46:47]
	v_cndmask_b32_e64 v9, v94, v9, s[46:47]
	s_nop 0
	v_mov_b32_dpp v94, v95 row_half_mirror row_mask:0xf bank_mask:0xf
	s_nop 1
	s_lshl_b64 s[26:27], s[26:27], 9
	s_ashr_i32 s29, s28, 31
	v_readlane_b32 s30, v96, 10
	s_add_u32 s66, s24, s62
	s_addc_u32 s67, s25, s63
	global_load_dwordx2 v[34:35], v121, s[66:67]
	s_waitcnt lgkmcnt(0)
	v_add_u32_dpp v9, v94, v9 quad_perm:[3,2,1,0] row_mask:0xf bank_mask:0xf
	s_nop 1
	s_lshl_b64 s[28:29], s[28:29], 9
	s_ashr_i32 s31, s30, 31
	v_readlane_b32 s34, v96, 11
	s_waitcnt lgkmcnt(0)
	v_add_u32_dpp v9, v9, v9 quad_perm:[2,3,0,1] row_mask:0xf bank_mask:0xf
	s_nop 1
	s_add_u32 s66, s26, s62
	s_addc_u32 s67, s27, s63
	global_load_dwordx2 v[36:37], v121, s[66:67]
	s_lshl_b64 s[30:31], s[30:31], 9
	s_ashr_i32 s35, s34, 31
	s_waitcnt lgkmcnt(0)
	v_add_u32_dpp v9, v9, v9 quad_perm:[1,0,3,2] row_mask:0xf bank_mask:0xf
	s_waitcnt vmcnt(10)
	v_mul_f32_e32 v7, v13, v7
	v_cvt_f32_i32_e32 v9, v9
	v_add_f32_e32 v9, v14, v9
	v_mul_f32_e32 v7, v7, v9
	v_mul_f32_e32 v9, 0x3d372713, v7
	v_mul_f32_e32 v9, v7, v9
	v_fma_f32 v9, v7, v9, v7
	v_mul_f32_e32 v9, 0x3fcc422a, v9
	v_mul_f32_e32 v9, 0xbfb8aa3b, v9
	v_exp_f32_e32 v9, v9
	v_readlane_b32 s38, v96, 12
	s_add_u32 s66, s28, s62
	s_addc_u32 s67, s29, s63
	global_load_dwordx2 v[38:39], v121, s[66:67]
	v_add_f32_e32 v9, 1.0, v9
	v_rcp_f32_e32 v9, v9
	s_lshl_b64 s[34:35], s[34:35], 9
	s_ashr_i32 s39, s38, 31
	v_pk_mul_f32 v[6:7], v[6:7], v[8:9]
	s_waitcnt vmcnt(28)
	v_alignbit_b32 v224, v92, v92, 4
	v_pk_mul_f32 v[6:7], v[6:7], v[6:7] op_sel:[0,1] op_sel_hi:[1,0]
	v_cvt_f16_f32_e32 v120, v6
	s_lshl_b64 s[38:39], s[38:39], 9
	v_readlane_b32 s50, v96, 13
	v_readlane_b32 s52, v96, 14
	v_readlane_b32 s54, v96, 15
	s_ashr_i32 s51, s50, 31
	s_ashr_i32 s53, s52, 31
	s_ashr_i32 s55, s54, 31
	s_lshl_b64 s[50:51], s[50:51], 9
	s_lshl_b64 s[52:53], s[52:53], 9
	s_lshl_b64 s[54:55], s[54:55], 9
	s_add_u32 s66, s30, s62
	s_addc_u32 s67, s31, s63
	global_load_dwordx2 v[40:41], v121, s[66:67]
	s_add_u32 s66, s34, s62
	s_addc_u32 s67, s35, s63
	global_load_dwordx2 v[60:61], v121, s[66:67]
	s_add_u32 s66, s38, s62
	s_addc_u32 s67, s39, s63
	global_load_dwordx2 v[58:59], v121, s[66:67]
	s_add_u32 s66, s50, s62
	s_addc_u32 s67, s51, s63
	global_load_dwordx2 v[56:57], v121, s[66:67]
	s_add_u32 s66, s52, s62
	s_addc_u32 s67, s53, s63
	global_load_dwordx2 v[54:55], v121, s[66:67]
	s_add_u32 s66, s54, s62
	s_addc_u32 s67, s55, s63
	global_load_dwordx2 v[52:53], v121, s[66:67]
	v_and_b32_e32 v8, 0x7070707, v92
	v_readlane_b32 s36, v120, 0
	v_and_b32_e32 v9, 0x7070707, v224
	v_perm_b32 v8, s2, v205, v8
	v_perm_b32 v9, s2, v205, v9
	v_and_or_b32 v8, v92, s4, v8
	v_and_or_b32 v9, v224, s4, v9
	v_perm_b32 v92, v9, v8, s5
	v_perm_b32 v94, v9, v8, s33
	v_perm_b32 v95, v9, v8, s0
	v_perm_b32 v8, v9, v8, s1
	v_pk_fma_f16 v8, v8, s36, v102 op_sel_hi:[1,0,1]
	v_alignbit_b32 v225, v93, v93, 4
	v_pk_fma_f16 v9, v92, s36, v105 op_sel_hi:[1,0,1]
	v_pk_fma_f16 v92, v94, s36, v104 op_sel_hi:[1,0,1]
	v_pk_fma_f16 v94, v95, s36, v103 op_sel_hi:[1,0,1]
	v_and_b32_e32 v95, 0x7070707, v93
	v_and_b32_e32 v102, 0x7070707, v225
	v_perm_b32 v95, s2, v205, v95
	v_perm_b32 v102, s2, v205, v102
	v_and_or_b32 v95, v93, s4, v95
	v_and_or_b32 v93, v225, s4, v102
	v_perm_b32 v102, v93, v95, s5
	v_perm_b32 v103, v93, v95, s33
	v_perm_b32 v104, v93, v95, s0
	v_perm_b32 v93, v93, v95, s1
	v_pk_fma_f16 v95, v102, s36, v101 op_sel_hi:[1,0,1]
	v_readlane_b32 s59, v120, 4
	s_waitcnt vmcnt(33)
	v_alignbit_b32 v224, v90, v90, 4
	v_pk_fma_f16 v100, v103, s36, v100 op_sel_hi:[1,0,1]
	v_pk_fma_f16 v99, v104, s36, v99 op_sel_hi:[1,0,1]
	v_pk_fma_f16 v7, v93, s36, v15 op_sel_hi:[1,0,1]
	s_setprio 0
	v_and_b32_e32 v93, 0x7070707, v90
	v_and_b32_e32 v101, 0x7070707, v224
	v_perm_b32 v93, s2, v205, v93
	v_perm_b32 v101, s2, v205, v101
	v_and_or_b32 v93, v90, s4, v93
	v_and_or_b32 v90, v224, s4, v101
	v_perm_b32 v103, v90, v93, s0
	v_perm_b32 v101, v90, v93, s5
	v_perm_b32 v102, v90, v93, s33
	v_perm_b32 v90, v90, v93, s1
	v_pk_fma_f16 v93, v103, s59, v94 op_sel_hi:[1,0,1]
	v_alignbit_b32 v225, v91, v91, 4
	v_pk_fma_f16 v8, v90, s59, v8 op_sel_hi:[1,0,1]
	v_and_b32_e32 v90, 0x7070707, v91
	v_and_b32_e32 v94, 0x7070707, v225
	v_pk_fma_f16 v9, v101, s59, v9 op_sel_hi:[1,0,1]
	v_perm_b32 v90, s2, v205, v90
	v_perm_b32 v94, s2, v205, v94
	v_and_or_b32 v90, v91, s4, v90
	v_and_or_b32 v91, v225, s4, v94
	v_pk_fma_f16 v92, v102, s59, v92 op_sel_hi:[1,0,1]
	v_perm_b32 v94, v91, v90, s5
	v_perm_b32 v102, v91, v90, s0
	v_perm_b32 v101, v91, v90, s33
	v_perm_b32 v90, v91, v90, s1
	v_pk_fma_f16 v91, v94, s59, v95 op_sel_hi:[1,0,1]
	v_pk_fma_f16 v95, v102, s59, v99 op_sel_hi:[1,0,1]
	v_readlane_b32 s60, v120, 8
	s_waitcnt vmcnt(32)
	v_alignbit_b32 v224, v88, v88, 4
	v_pk_fma_f16 v94, v101, s59, v100 op_sel_hi:[1,0,1]
	v_pk_fma_f16 v7, v90, s59, v7 op_sel_hi:[1,0,1]
	v_and_b32_e32 v90, 0x7070707, v88
	v_and_b32_e32 v99, 0x7070707, v224
	v_perm_b32 v90, s2, v205, v90
	v_perm_b32 v99, s2, v205, v99
	v_and_or_b32 v90, v88, s4, v90
	v_and_or_b32 v88, v224, s4, v99
	v_perm_b32 v100, v88, v90, s33
	v_perm_b32 v101, v88, v90, s0
	v_perm_b32 v99, v88, v90, s5
	v_perm_b32 v88, v88, v90, s1
	v_pk_fma_f16 v90, v100, s60, v92 op_sel_hi:[1,0,1]
	v_pk_fma_f16 v92, v101, s60, v93 op_sel_hi:[1,0,1]
	v_alignbit_b32 v225, v89, v89, 4
	v_pk_fma_f16 v8, v88, s60, v8 op_sel_hi:[1,0,1]
	v_and_b32_e32 v88, 0x7070707, v89
	v_and_b32_e32 v93, 0x7070707, v225
	v_pk_fma_f16 v9, v99, s60, v9 op_sel_hi:[1,0,1]
	v_perm_b32 v88, s2, v205, v88
	v_perm_b32 v93, s2, v205, v93
	v_and_or_b32 v88, v89, s4, v88
	v_and_or_b32 v89, v225, s4, v93
	v_perm_b32 v93, v89, v88, s5
	v_perm_b32 v99, v89, v88, s33
	v_perm_b32 v100, v89, v88, s0
	v_perm_b32 v88, v89, v88, s1
	v_pk_fma_f16 v89, v93, s60, v91 op_sel_hi:[1,0,1]
	v_pk_fma_f16 v91, v99, s60, v94 op_sel_hi:[1,0,1]
	v_readlane_b32 s36, v120, 12
	s_waitcnt vmcnt(31)
	v_alignbit_b32 v224, v86, v86, 4
	v_pk_fma_f16 v93, v100, s60, v95 op_sel_hi:[1,0,1]
	v_pk_fma_f16 v7, v88, s60, v7 op_sel_hi:[1,0,1]
	v_and_b32_e32 v88, 0x7070707, v86
	v_and_b32_e32 v94, 0x7070707, v224
	v_perm_b32 v88, s2, v205, v88
	v_perm_b32 v94, s2, v205, v94
	v_and_or_b32 v88, v86, s4, v88
	v_and_or_b32 v86, v224, s4, v94
	v_perm_b32 v95, v86, v88, s33
	v_perm_b32 v99, v86, v88, s0
	v_perm_b32 v94, v86, v88, s5
	v_perm_b32 v86, v86, v88, s1
	v_pk_fma_f16 v88, v95, s36, v90 op_sel_hi:[1,0,1]
	v_pk_fma_f16 v90, v99, s36, v92 op_sel_hi:[1,0,1]
	v_alignbit_b32 v225, v87, v87, 4
	v_pk_fma_f16 v8, v86, s36, v8 op_sel_hi:[1,0,1]
	v_and_b32_e32 v86, 0x7070707, v87
	v_and_b32_e32 v92, 0x7070707, v225
	v_pk_fma_f16 v9, v94, s36, v9 op_sel_hi:[1,0,1]
	v_perm_b32 v86, s2, v205, v86
	v_perm_b32 v92, s2, v205, v92
	v_and_or_b32 v86, v87, s4, v86
	v_and_or_b32 v87, v225, s4, v92
	v_perm_b32 v92, v87, v86, s5
	v_perm_b32 v94, v87, v86, s33
	v_perm_b32 v95, v87, v86, s0
	v_perm_b32 v86, v87, v86, s1
	v_pk_fma_f16 v87, v92, s36, v89 op_sel_hi:[1,0,1]
	v_readlane_b32 s59, v120, 16
	s_waitcnt vmcnt(30)
	v_alignbit_b32 v224, v84, v84, 4
	v_pk_fma_f16 v89, v94, s36, v91 op_sel_hi:[1,0,1]
	v_pk_fma_f16 v91, v95, s36, v93 op_sel_hi:[1,0,1]
	v_pk_fma_f16 v7, v86, s36, v7 op_sel_hi:[1,0,1]
	v_and_b32_e32 v86, 0x7070707, v84
	v_and_b32_e32 v92, 0x7070707, v224
	v_perm_b32 v86, s2, v205, v86
	v_perm_b32 v92, s2, v205, v92
	v_and_or_b32 v86, v84, s4, v86
	v_and_or_b32 v84, v224, s4, v92
	v_perm_b32 v93, v84, v86, s33
	v_perm_b32 v94, v84, v86, s0
	v_perm_b32 v92, v84, v86, s5
	v_perm_b32 v84, v84, v86, s1
	v_pk_fma_f16 v86, v93, s59, v88 op_sel_hi:[1,0,1]
	v_pk_fma_f16 v88, v94, s59, v90 op_sel_hi:[1,0,1]
	v_alignbit_b32 v225, v85, v85, 4
	v_pk_fma_f16 v8, v84, s59, v8 op_sel_hi:[1,0,1]
	v_and_b32_e32 v84, 0x7070707, v85
	v_and_b32_e32 v90, 0x7070707, v225
	v_pk_fma_f16 v9, v92, s59, v9 op_sel_hi:[1,0,1]
	v_perm_b32 v84, s2, v205, v84
	v_perm_b32 v90, s2, v205, v90
	v_and_or_b32 v84, v85, s4, v84
	v_and_or_b32 v85, v225, s4, v90
	v_perm_b32 v90, v85, v84, s5
	v_perm_b32 v92, v85, v84, s33
	v_perm_b32 v93, v85, v84, s0
	v_perm_b32 v84, v85, v84, s1
	v_pk_fma_f16 v85, v90, s59, v87 op_sel_hi:[1,0,1]
	v_readlane_b32 s60, v120, 20
	s_waitcnt vmcnt(29)
	v_alignbit_b32 v224, v82, v82, 4
	v_pk_fma_f16 v87, v92, s59, v89 op_sel_hi:[1,0,1]
	v_pk_fma_f16 v89, v93, s59, v91 op_sel_hi:[1,0,1]
	v_pk_fma_f16 v7, v84, s59, v7 op_sel_hi:[1,0,1]
	v_and_b32_e32 v84, 0x7070707, v82
	v_and_b32_e32 v90, 0x7070707, v224
	v_perm_b32 v84, s2, v205, v84
	v_perm_b32 v90, s2, v205, v90
	v_and_or_b32 v84, v82, s4, v84
	v_and_or_b32 v82, v224, s4, v90
	v_perm_b32 v91, v82, v84, s33
	v_perm_b32 v92, v82, v84, s0
	v_perm_b32 v90, v82, v84, s5
	v_perm_b32 v82, v82, v84, s1
	v_pk_fma_f16 v84, v91, s60, v86 op_sel_hi:[1,0,1]
	v_pk_fma_f16 v86, v92, s60, v88 op_sel_hi:[1,0,1]
	s_add_u32 s66, s10, s64
	s_addc_u32 s67, s11, s65
	global_load_dwordx2 v[92:93], v121, s[66:67]
	v_alignbit_b32 v225, v83, v83, 4
	v_pk_fma_f16 v8, v82, s60, v8 op_sel_hi:[1,0,1]
	v_and_b32_e32 v82, 0x7070707, v83
	v_and_b32_e32 v88, 0x7070707, v225
	v_pk_fma_f16 v9, v90, s60, v9 op_sel_hi:[1,0,1]
	v_perm_b32 v82, s2, v205, v82
	v_perm_b32 v88, s2, v205, v88
	v_and_or_b32 v82, v83, s4, v82
	v_and_or_b32 v83, v225, s4, v88
	v_perm_b32 v88, v83, v82, s5
	v_perm_b32 v90, v83, v82, s33
	v_perm_b32 v91, v83, v82, s0
	v_perm_b32 v82, v83, v82, s1
	v_pk_fma_f16 v83, v88, s60, v85 op_sel_hi:[1,0,1]
	v_readlane_b32 s36, v120, 24
	s_waitcnt vmcnt(29)
	v_alignbit_b32 v224, v80, v80, 4
	v_pk_fma_f16 v85, v90, s60, v87 op_sel_hi:[1,0,1]
	v_pk_fma_f16 v87, v91, s60, v89 op_sel_hi:[1,0,1]
	v_pk_fma_f16 v7, v82, s60, v7 op_sel_hi:[1,0,1]
	v_and_b32_e32 v82, 0x7070707, v80
	v_and_b32_e32 v88, 0x7070707, v224
	v_perm_b32 v82, s2, v205, v82
	v_perm_b32 v88, s2, v205, v88
	v_and_or_b32 v82, v80, s4, v82
	v_and_or_b32 v80, v224, s4, v88
	v_perm_b32 v89, v80, v82, s33
	v_perm_b32 v90, v80, v82, s0
	v_perm_b32 v88, v80, v82, s5
	v_perm_b32 v80, v80, v82, s1
	v_pk_fma_f16 v82, v89, s36, v84 op_sel_hi:[1,0,1]
	v_pk_fma_f16 v84, v90, s36, v86 op_sel_hi:[1,0,1]
	s_add_u32 s66, s12, s64
	s_addc_u32 s67, s13, s65
	global_load_dwordx2 v[90:91], v121, s[66:67]
	v_alignbit_b32 v225, v81, v81, 4
	v_pk_fma_f16 v8, v80, s36, v8 op_sel_hi:[1,0,1]
	v_and_b32_e32 v80, 0x7070707, v81
	v_and_b32_e32 v86, 0x7070707, v225
	v_pk_fma_f16 v9, v88, s36, v9 op_sel_hi:[1,0,1]
	v_perm_b32 v80, s2, v205, v80
	v_perm_b32 v86, s2, v205, v86
	v_and_or_b32 v80, v81, s4, v80
	v_and_or_b32 v81, v225, s4, v86
	v_perm_b32 v86, v81, v80, s5
	v_perm_b32 v88, v81, v80, s33
	v_perm_b32 v89, v81, v80, s0
	v_perm_b32 v80, v81, v80, s1
	v_pk_fma_f16 v81, v86, s36, v83 op_sel_hi:[1,0,1]
	v_readlane_b32 s59, v120, 28
	s_waitcnt vmcnt(29)
	v_alignbit_b32 v224, v78, v78, 4
	v_pk_fma_f16 v83, v88, s36, v85 op_sel_hi:[1,0,1]
	v_pk_fma_f16 v85, v89, s36, v87 op_sel_hi:[1,0,1]
	v_pk_fma_f16 v7, v80, s36, v7 op_sel_hi:[1,0,1]
	v_and_b32_e32 v80, 0x7070707, v78
	v_and_b32_e32 v86, 0x7070707, v224
	v_perm_b32 v80, s2, v205, v80
	v_perm_b32 v86, s2, v205, v86
	v_and_or_b32 v80, v78, s4, v80
	v_and_or_b32 v78, v224, s4, v86
	v_perm_b32 v87, v78, v80, s33
	v_perm_b32 v88, v78, v80, s0
	v_perm_b32 v86, v78, v80, s5
	v_perm_b32 v78, v78, v80, s1
	v_pk_fma_f16 v80, v87, s59, v82 op_sel_hi:[1,0,1]
	v_pk_fma_f16 v82, v88, s59, v84 op_sel_hi:[1,0,1]
	s_add_u32 s66, s14, s64
	s_addc_u32 s67, s15, s65
	global_load_dwordx2 v[88:89], v121, s[66:67]
	v_alignbit_b32 v225, v79, v79, 4
	v_pk_fma_f16 v8, v78, s59, v8 op_sel_hi:[1,0,1]
	v_and_b32_e32 v78, 0x7070707, v79
	v_and_b32_e32 v84, 0x7070707, v225
	v_pk_fma_f16 v9, v86, s59, v9 op_sel_hi:[1,0,1]
	v_perm_b32 v78, s2, v205, v78
	v_perm_b32 v84, s2, v205, v84
	v_and_or_b32 v78, v79, s4, v78
	v_and_or_b32 v79, v225, s4, v84
	v_perm_b32 v84, v79, v78, s5
	v_perm_b32 v86, v79, v78, s33
	v_perm_b32 v87, v79, v78, s0
	v_perm_b32 v78, v79, v78, s1
	v_pk_fma_f16 v79, v84, s59, v81 op_sel_hi:[1,0,1]
	v_readlane_b32 s60, v120, 32
	s_waitcnt vmcnt(29)
	v_alignbit_b32 v224, v76, v76, 4
	v_pk_fma_f16 v81, v86, s59, v83 op_sel_hi:[1,0,1]
	v_pk_fma_f16 v83, v87, s59, v85 op_sel_hi:[1,0,1]
	v_pk_fma_f16 v7, v78, s59, v7 op_sel_hi:[1,0,1]
	v_and_b32_e32 v78, 0x7070707, v76
	v_and_b32_e32 v84, 0x7070707, v224
	v_perm_b32 v78, s2, v205, v78
	v_perm_b32 v84, s2, v205, v84
	v_and_or_b32 v78, v76, s4, v78
	v_and_or_b32 v76, v224, s4, v84
	v_perm_b32 v85, v76, v78, s33
	v_perm_b32 v86, v76, v78, s0
	v_perm_b32 v84, v76, v78, s5
	v_perm_b32 v76, v76, v78, s1
	v_pk_fma_f16 v78, v85, s60, v80 op_sel_hi:[1,0,1]
	v_pk_fma_f16 v80, v86, s60, v82 op_sel_hi:[1,0,1]
	s_add_u32 s66, s16, s64
	s_addc_u32 s67, s17, s65
	global_load_dwordx2 v[86:87], v121, s[66:67]
	v_alignbit_b32 v225, v77, v77, 4
	v_pk_fma_f16 v8, v76, s60, v8 op_sel_hi:[1,0,1]
	v_and_b32_e32 v76, 0x7070707, v77
	v_and_b32_e32 v82, 0x7070707, v225
	v_pk_fma_f16 v9, v84, s60, v9 op_sel_hi:[1,0,1]
	v_perm_b32 v76, s2, v205, v76
	v_perm_b32 v82, s2, v205, v82
	v_and_or_b32 v76, v77, s4, v76
	v_and_or_b32 v77, v225, s4, v82
	v_perm_b32 v82, v77, v76, s5
	v_perm_b32 v84, v77, v76, s33
	v_perm_b32 v85, v77, v76, s0
	v_perm_b32 v76, v77, v76, s1
	v_pk_fma_f16 v77, v82, s60, v79 op_sel_hi:[1,0,1]
	v_readlane_b32 s36, v120, 36
	s_waitcnt vmcnt(28)
	v_alignbit_b32 v224, v70, v70, 4
	v_pk_fma_f16 v79, v84, s60, v81 op_sel_hi:[1,0,1]
	v_pk_fma_f16 v81, v85, s60, v83 op_sel_hi:[1,0,1]
	v_pk_fma_f16 v7, v76, s60, v7 op_sel_hi:[1,0,1]
	v_and_b32_e32 v76, 0x7070707, v70
	v_and_b32_e32 v82, 0x7070707, v224
	v_perm_b32 v76, s2, v205, v76
	v_perm_b32 v82, s2, v205, v82
	v_and_or_b32 v76, v70, s4, v76
	v_and_or_b32 v70, v224, s4, v82
	v_perm_b32 v83, v70, v76, s33
	v_perm_b32 v84, v70, v76, s0
	v_perm_b32 v82, v70, v76, s5
	v_perm_b32 v70, v70, v76, s1
	v_pk_fma_f16 v76, v83, s36, v78 op_sel_hi:[1,0,1]
	v_pk_fma_f16 v78, v84, s36, v80 op_sel_hi:[1,0,1]
	s_add_u32 s66, s18, s64
	s_addc_u32 s67, s19, s65
	global_load_dwordx2 v[84:85], v121, s[66:67]
	v_alignbit_b32 v225, v71, v71, 4
	v_pk_fma_f16 v8, v70, s36, v8 op_sel_hi:[1,0,1]
	v_and_b32_e32 v70, 0x7070707, v71
	v_and_b32_e32 v80, 0x7070707, v225
	v_pk_fma_f16 v9, v82, s36, v9 op_sel_hi:[1,0,1]
	v_perm_b32 v70, s2, v205, v70
	v_perm_b32 v80, s2, v205, v80
	v_and_or_b32 v70, v71, s4, v70
	v_and_or_b32 v71, v225, s4, v80
	v_perm_b32 v80, v71, v70, s5
	v_perm_b32 v82, v71, v70, s33
	v_perm_b32 v83, v71, v70, s0
	v_perm_b32 v70, v71, v70, s1
	v_pk_fma_f16 v71, v80, s36, v77 op_sel_hi:[1,0,1]
	v_readlane_b32 s59, v120, 40
	s_waitcnt vmcnt(25)
	v_alignbit_b32 v224, v66, v66, 4
	v_pk_fma_f16 v77, v82, s36, v79 op_sel_hi:[1,0,1]
	v_pk_fma_f16 v79, v83, s36, v81 op_sel_hi:[1,0,1]
	v_pk_fma_f16 v7, v70, s36, v7 op_sel_hi:[1,0,1]
	v_and_b32_e32 v70, 0x7070707, v66
	v_and_b32_e32 v80, 0x7070707, v224
	v_perm_b32 v70, s2, v205, v70
	v_perm_b32 v80, s2, v205, v80
	v_and_or_b32 v70, v66, s4, v70
	v_and_or_b32 v66, v224, s4, v80
	v_perm_b32 v81, v66, v70, s33
	v_perm_b32 v82, v66, v70, s0
	v_perm_b32 v80, v66, v70, s5
	v_perm_b32 v66, v66, v70, s1
	v_pk_fma_f16 v70, v81, s59, v76 op_sel_hi:[1,0,1]
	v_pk_fma_f16 v76, v82, s59, v78 op_sel_hi:[1,0,1]
	s_add_u32 s66, s20, s64
	s_addc_u32 s67, s21, s65
	global_load_dwordx2 v[82:83], v121, s[66:67]
	v_alignbit_b32 v225, v67, v67, 4
	v_pk_fma_f16 v8, v66, s59, v8 op_sel_hi:[1,0,1]
	v_and_b32_e32 v66, 0x7070707, v67
	v_and_b32_e32 v78, 0x7070707, v225
	v_pk_fma_f16 v9, v80, s59, v9 op_sel_hi:[1,0,1]
	v_perm_b32 v66, s2, v205, v66
	v_perm_b32 v78, s2, v205, v78
	v_and_or_b32 v66, v67, s4, v66
	v_and_or_b32 v67, v225, s4, v78
	v_perm_b32 v78, v67, v66, s5
	v_perm_b32 v80, v67, v66, s33
	v_perm_b32 v81, v67, v66, s0
	v_perm_b32 v66, v67, v66, s1
	v_pk_fma_f16 v67, v78, s59, v71 op_sel_hi:[1,0,1]
	v_readlane_b32 s60, v120, 44
	s_waitcnt vmcnt(31)
	v_alignbit_b32 v224, v72, v72, 4
	v_pk_fma_f16 v71, v80, s59, v77 op_sel_hi:[1,0,1]
	v_pk_fma_f16 v77, v81, s59, v79 op_sel_hi:[1,0,1]
	v_pk_fma_f16 v7, v66, s59, v7 op_sel_hi:[1,0,1]
	v_and_b32_e32 v66, 0x7070707, v72
	v_and_b32_e32 v78, 0x7070707, v224
	v_perm_b32 v66, s2, v205, v66
	v_perm_b32 v78, s2, v205, v78
	v_and_or_b32 v66, v72, s4, v66
	v_and_or_b32 v72, v224, s4, v78
	v_perm_b32 v80, v72, v66, s0
	v_perm_b32 v78, v72, v66, s5
	v_perm_b32 v79, v72, v66, s33
	v_perm_b32 v66, v72, v66, s1
	v_pk_fma_f16 v72, v80, s60, v76 op_sel_hi:[1,0,1]
	s_add_u32 s66, s22, s64
	s_addc_u32 s67, s23, s65
	global_load_dwordx2 v[80:81], v121, s[66:67]
	v_alignbit_b32 v225, v73, v73, 4
	v_pk_fma_f16 v8, v66, s60, v8 op_sel_hi:[1,0,1]
	v_and_b32_e32 v66, 0x7070707, v73
	v_and_b32_e32 v76, 0x7070707, v225
	v_pk_fma_f16 v9, v78, s60, v9 op_sel_hi:[1,0,1]
	v_perm_b32 v66, s2, v205, v66
	v_perm_b32 v76, s2, v205, v76
	v_and_or_b32 v66, v73, s4, v66
	v_and_or_b32 v73, v225, s4, v76
	v_perm_b32 v76, v73, v66, s5
	v_pk_fma_f16 v70, v79, s60, v70 op_sel_hi:[1,0,1]
	v_perm_b32 v78, v73, v66, s33
	v_perm_b32 v79, v73, v66, s0
	v_perm_b32 v66, v73, v66, s1
	v_pk_fma_f16 v67, v76, s60, v67 op_sel_hi:[1,0,1]
	v_readlane_b32 s36, v120, 48
	s_waitcnt vmcnt(30)
	v_alignbit_b32 v224, v68, v68, 4
	v_pk_fma_f16 v71, v78, s60, v71 op_sel_hi:[1,0,1]
	v_pk_fma_f16 v73, v79, s60, v77 op_sel_hi:[1,0,1]
	v_pk_fma_f16 v7, v66, s60, v7 op_sel_hi:[1,0,1]
	v_and_b32_e32 v66, 0x7070707, v68
	v_and_b32_e32 v76, 0x7070707, v224
	v_perm_b32 v66, s2, v205, v66
	v_perm_b32 v76, s2, v205, v76
	v_and_or_b32 v66, v68, s4, v66
	v_and_or_b32 v68, v224, s4, v76
	v_perm_b32 v77, v68, v66, s33
	v_perm_b32 v78, v68, v66, s0
	v_perm_b32 v76, v68, v66, s5
	v_perm_b32 v66, v68, v66, s1
	v_pk_fma_f16 v68, v77, s36, v70 op_sel_hi:[1,0,1]
	v_pk_fma_f16 v70, v78, s36, v72 op_sel_hi:[1,0,1]
	s_add_u32 s66, s24, s64
	s_addc_u32 s67, s25, s65
	global_load_dwordx2 v[78:79], v121, s[66:67]
	v_alignbit_b32 v225, v69, v69, 4
	v_pk_fma_f16 v8, v66, s36, v8 op_sel_hi:[1,0,1]
	v_and_b32_e32 v66, 0x7070707, v69
	v_and_b32_e32 v72, 0x7070707, v225
	v_pk_fma_f16 v9, v76, s36, v9 op_sel_hi:[1,0,1]
	v_perm_b32 v66, s2, v205, v66
	v_perm_b32 v72, s2, v205, v72
	v_and_or_b32 v66, v69, s4, v66
	v_and_or_b32 v69, v225, s4, v72
	v_perm_b32 v72, v69, v66, s5
	v_perm_b32 v76, v69, v66, s33
	v_perm_b32 v77, v69, v66, s0
	v_perm_b32 v66, v69, v66, s1
	v_pk_fma_f16 v67, v72, s36, v67 op_sel_hi:[1,0,1]
	v_readlane_b32 s59, v120, 52
	s_waitcnt vmcnt(29)
	v_alignbit_b32 v224, v64, v64, 4
	v_pk_fma_f16 v69, v76, s36, v71 op_sel_hi:[1,0,1]
	v_pk_fma_f16 v71, v77, s36, v73 op_sel_hi:[1,0,1]
	v_pk_fma_f16 v7, v66, s36, v7 op_sel_hi:[1,0,1]
	v_and_b32_e32 v66, 0x7070707, v64
	v_and_b32_e32 v72, 0x7070707, v224
	v_perm_b32 v66, s2, v205, v66
	v_perm_b32 v72, s2, v205, v72
	v_and_or_b32 v66, v64, s4, v66
	v_and_or_b32 v64, v224, s4, v72
	v_perm_b32 v73, v64, v66, s33
	v_perm_b32 v76, v64, v66, s0
	v_perm_b32 v72, v64, v66, s5
	v_perm_b32 v64, v64, v66, s1
	v_pk_fma_f16 v66, v73, s59, v68 op_sel_hi:[1,0,1]
	v_pk_fma_f16 v68, v76, s59, v70 op_sel_hi:[1,0,1]
	s_add_u32 s66, s26, s64
	s_addc_u32 s67, s27, s65
	global_load_dwordx2 v[76:77], v121, s[66:67]
	v_alignbit_b32 v225, v65, v65, 4
	v_pk_fma_f16 v8, v64, s59, v8 op_sel_hi:[1,0,1]
	v_and_b32_e32 v64, 0x7070707, v65
	v_and_b32_e32 v70, 0x7070707, v225
	v_pk_fma_f16 v9, v72, s59, v9 op_sel_hi:[1,0,1]
	v_perm_b32 v64, s2, v205, v64
	v_perm_b32 v70, s2, v205, v70
	v_and_or_b32 v64, v65, s4, v64
	v_and_or_b32 v65, v225, s4, v70
	v_perm_b32 v70, v65, v64, s5
	v_perm_b32 v72, v65, v64, s33
	v_perm_b32 v73, v65, v64, s0
	v_perm_b32 v64, v65, v64, s1
	v_pk_fma_f16 v65, v70, s59, v67 op_sel_hi:[1,0,1]
	v_readlane_b32 s60, v120, 56
	s_waitcnt vmcnt(31)
	v_alignbit_b32 v224, v62, v62, 4
	v_pk_fma_f16 v67, v72, s59, v69 op_sel_hi:[1,0,1]
	v_pk_fma_f16 v69, v73, s59, v71 op_sel_hi:[1,0,1]
	v_pk_fma_f16 v7, v64, s59, v7 op_sel_hi:[1,0,1]
	v_and_b32_e32 v64, 0x7070707, v62
	v_and_b32_e32 v70, 0x7070707, v224
	v_perm_b32 v64, s2, v205, v64
	v_perm_b32 v70, s2, v205, v70
	v_and_or_b32 v64, v62, s4, v64
	v_and_or_b32 v62, v224, s4, v70
	v_perm_b32 v71, v62, v64, s33
	v_perm_b32 v72, v62, v64, s0
	v_perm_b32 v70, v62, v64, s5
	v_perm_b32 v62, v62, v64, s1
	v_pk_fma_f16 v64, v71, s60, v66 op_sel_hi:[1,0,1]
	v_pk_fma_f16 v66, v72, s60, v68 op_sel_hi:[1,0,1]
	s_add_u32 s66, s34, s64
	s_addc_u32 s67, s35, s65
	global_load_dwordx2 v[72:73], v121, s[66:67]
	v_alignbit_b32 v225, v63, v63, 4
	v_pk_fma_f16 v8, v62, s60, v8 op_sel_hi:[1,0,1]
	v_and_b32_e32 v62, 0x7070707, v63
	v_and_b32_e32 v68, 0x7070707, v225
	v_pk_fma_f16 v9, v70, s60, v9 op_sel_hi:[1,0,1]
	v_perm_b32 v62, s2, v205, v62
	v_perm_b32 v68, s2, v205, v68
	v_and_or_b32 v62, v63, s4, v62
	v_and_or_b32 v63, v225, s4, v68
	v_perm_b32 v68, v63, v62, s5
	v_perm_b32 v70, v63, v62, s33
	v_perm_b32 v71, v63, v62, s0
	v_perm_b32 v62, v63, v62, s1
	v_pk_fma_f16 v7, v62, s60, v7 op_sel_hi:[1,0,1]
	v_readlane_b32 s36, v120, 60
	s_waitcnt vmcnt(29)
	v_alignbit_b32 v224, v50, v50, 4
	v_pk_fma_f16 v63, v68, s60, v65 op_sel_hi:[1,0,1]
	v_pk_fma_f16 v65, v70, s60, v67 op_sel_hi:[1,0,1]
	v_pk_fma_f16 v67, v71, s60, v69 op_sel_hi:[1,0,1]
	s_add_u32 s66, s28, s64
	s_addc_u32 s67, s29, s65
	global_load_dwordx2 v[70:71], v121, s[66:67]
	v_and_b32_e32 v15, 0x7070707, v50
	v_and_b32_e32 v62, 0x7070707, v224
	v_perm_b32 v15, s2, v205, v15
	v_perm_b32 v62, s2, v205, v62
	v_and_or_b32 v15, v50, s4, v15
	v_and_or_b32 v50, v224, s4, v62
	v_perm_b32 v62, v50, v15, s5
	v_perm_b32 v68, v50, v15, s33
	v_perm_b32 v69, v50, v15, s0
	v_perm_b32 v15, v50, v15, s1
	v_pk_fma_f16 v105, v62, s36, v9 op_sel_hi:[1,0,1]
	v_alignbit_b32 v225, v51, v51, 4
	v_pk_fma_f16 v102, v15, s36, v8 op_sel_hi:[1,0,1]
	v_and_b32_e32 v8, 0x7070707, v51
	v_and_b32_e32 v9, 0x7070707, v225
	v_perm_b32 v8, s2, v205, v8
	v_perm_b32 v9, s2, v205, v9
	v_and_or_b32 v8, v51, s4, v8
	v_and_or_b32 v9, v225, s4, v9
	v_perm_b32 v15, v9, v8, s5
	v_perm_b32 v50, v9, v8, s33
	v_perm_b32 v51, v9, v8, s0
	v_perm_b32 v8, v9, v8, s1
	v_pk_fma_f16 v104, v68, s36, v64 op_sel_hi:[1,0,1]
	v_pk_fma_f16 v103, v69, s36, v66 op_sel_hi:[1,0,1]
	s_add_u32 s66, s38, s64
	s_addc_u32 s67, s39, s65
	global_load_dwordx2 v[68:69], v121, s[66:67]
	v_pk_fma_f16 v101, v15, s36, v63 op_sel_hi:[1,0,1]
	s_add_u32 s66, s52, s64
	s_addc_u32 s67, s53, s65
	global_load_dwordx2 v[62:63], v121, s[66:67]
	v_pk_fma_f16 v100, v50, s36, v65 op_sel_hi:[1,0,1]
	s_add_u32 s66, s50, s64
	s_addc_u32 s67, s51, s65
	global_load_dwordx2 v[64:65], v121, s[66:67]
	v_pk_fma_f16 v99, v51, s36, v67 op_sel_hi:[1,0,1]
	s_add_u32 s66, s30, s64
	s_addc_u32 s67, s31, s65
	global_load_dwordx2 v[66:67], v121, s[66:67]
	s_add_u32 s66, s54, s64
	s_addc_u32 s67, s55, s65
	global_load_dwordx2 v[50:51], v121, s[66:67]
	v_pk_fma_f16 v15, v8, s36, v7 op_sel_hi:[1,0,1]
	s_cmpk_eq_i32 s56, 0x90
	s_cbranch_scc0 .LBB0_770
	v_lshl_add_u64 v[94:95], v[2:3], 2, v[44:45]
	v_mov_b32_e32 v106, v208
	v_mov_b32_e32 v107, v209
	v_mov_b32_e32 v108, v210
	v_mov_b32_e32 v109, v211
	v_mov_b32_e32 v8, v212
	v_mov_b32_e32 v9, v213
	v_mov_b32_e32 v10, v214
	v_mov_b32_e32 v11, v215
	v_mov_b32_e32 v4, v216
	v_mov_b32_e32 v5, v217
	v_mov_b32_e32 v6, v218
	v_mov_b32_e32 v7, v219
	v_mov_b32_e32 v0, v220
	v_mov_b32_e32 v1, v221
	v_mov_b32_e32 v2, v222
	v_mov_b32_e32 v3, v223
	v_cvt_f32_f16_sdwa v13, v105 dst_sel:DWORD dst_unused:UNUSED_PAD src0_sel:WORD_1
	v_cvt_f32_f16_e32 v12, v105
	s_mov_b32 s12, 0x800000
	v_readlane_b32 s10, v255, 5
	v_readlane_b32 s11, v255, 6
	v_pk_add_f32 v[0:1], v[0:1], v[12:13]
	v_cvt_f32_f16_sdwa v13, v104 dst_sel:DWORD dst_unused:UNUSED_PAD src0_sel:WORD_1
	v_cvt_f32_f16_e32 v12, v104
	v_lshl_add_u64 v[48:49], v[48:49], 0, s[10:11]
	v_pk_add_f32 v[2:3], v[2:3], v[12:13]
	v_cvt_f32_f16_sdwa v13, v103 dst_sel:DWORD dst_unused:UNUSED_PAD src0_sel:WORD_1
	v_cvt_f32_f16_e32 v12, v103
	global_store_dwordx4 v[94:95], v[0:3], off
	v_pk_add_f32 v[4:5], v[4:5], v[12:13]
	v_cvt_f32_f16_sdwa v13, v102 dst_sel:DWORD dst_unused:UNUSED_PAD src0_sel:WORD_1
	v_cvt_f32_f16_e32 v12, v102
	v_mov_b32_e32 v102, v1
	v_mov_b32_e32 v103, v5
	v_pk_mul_f32 v[102:103], v[102:103], v[102:103]
	v_pk_add_f32 v[6:7], v[6:7], v[12:13]
	v_mov_b32_e32 v12, v0
	v_mov_b32_e32 v13, v4
	v_pk_fma_f32 v[12:13], v[12:13], v[12:13], v[102:103]
	v_mov_b32_e32 v102, v2
	v_mov_b32_e32 v103, v6
	v_pk_fma_f32 v[12:13], v[102:103], v[102:103], v[12:13]
	v_mov_b32_e32 v102, v3
	v_mov_b32_e32 v103, v7
	v_pk_fma_f32 v[102:103], v[102:103], v[102:103], v[12:13]
	v_cvt_f32_f16_sdwa v13, v101 dst_sel:DWORD dst_unused:UNUSED_PAD src0_sel:WORD_1
	v_cvt_f32_f16_e32 v12, v101
	v_cvt_f32_f16_sdwa v101, v15 dst_sel:DWORD dst_unused:UNUSED_PAD src0_sel:WORD_1
	global_store_dwordx4 v[94:95], v[4:7], off offset:16
	v_pk_add_f32 v[8:9], v[8:9], v[12:13]
	v_cvt_f32_f16_sdwa v13, v100 dst_sel:DWORD dst_unused:UNUSED_PAD src0_sel:WORD_1
	v_cvt_f32_f16_e32 v12, v100
	v_cvt_f32_f16_e32 v100, v15
	v_pk_add_f32 v[10:11], v[10:11], v[12:13]
	v_cvt_f32_f16_sdwa v13, v99 dst_sel:DWORD dst_unused:UNUSED_PAD src0_sel:WORD_1
	v_cvt_f32_f16_e32 v12, v99
	v_pk_add_f32 v[14:15], v[108:109], v[100:101]
	v_mov_b32_e32 v100, v9
	global_store_dwordx4 v[94:95], v[8:11], off offset:32
	v_pk_add_f32 v[12:13], v[106:107], v[12:13]
	global_store_dwordx4 v[94:95], v[12:15], off offset:48
	v_mov_b32_e32 v101, v13
	v_mov_b32_e32 v94, v8
	v_mov_b32_e32 v95, v12
	v_pk_mul_f32 v[100:101], v[100:101], v[100:101]
	v_add_f32_e32 v99, v102, v103
	v_pk_fma_f32 v[94:95], v[94:95], v[94:95], v[100:101]
	v_mov_b32_e32 v100, v10
	v_mov_b32_e32 v101, v14
	v_pk_fma_f32 v[94:95], v[100:101], v[100:101], v[94:95]
	v_mov_b32_e32 v100, v11
	v_mov_b32_e32 v101, v15
	v_pk_fma_f32 v[94:95], v[100:101], v[100:101], v[94:95]
	global_load_dwordx4 v[100:103], v[46:47], off offset:48
	global_load_dwordx4 v[104:107], v[46:47], off offset:32
	global_load_dwordx4 v[108:111], v[46:47], off offset:16
	global_load_dwordx4 v[112:115], v[46:47], off
	v_add_f32_e32 v94, v99, v94
	v_add_f32_e32 v94, v94, v95
	v_mov_b32_e32 v95, v94
	s_nop 1
	v_permlane32_swap_b32 v95, v94
	s_waitcnt lgkmcnt(0)
	v_add_f32_e32 v94, v94, v95
	v_mov_b32_e32 v95, v94
	s_nop 1
	v_permlane16_swap_b32 v95, v94
	s_waitcnt lgkmcnt(0)
	v_add_f32_e32 v94, v94, v95
	s_nop 1
	v_mov_b32_dpp v95, v94 row_ror:8 row_mask:0xf bank_mask:0xf
	s_waitcnt lgkmcnt(0)
	v_add_f32_e32 v94, v94, v95
	s_nop 1
	v_mov_b32_dpp v95, v94 row_half_mirror row_mask:0xf bank_mask:0xf
	s_nop 1
	v_mov_b32_dpp v95, v95 quad_perm:[3,2,1,0] row_mask:0xf bank_mask:0xf
	s_waitcnt lgkmcnt(0)
	v_add_f32_e32 v94, v94, v95
	s_nop 1
	v_mov_b32_dpp v95, v94 quad_perm:[2,3,0,1] row_mask:0xf bank_mask:0xf
	s_waitcnt lgkmcnt(0)
	v_add_f32_e32 v94, v94, v95
	s_nop 1
	v_mov_b32_dpp v95, v94 quad_perm:[1,0,3,2] row_mask:0xf bank_mask:0xf
	s_waitcnt lgkmcnt(0)
	v_add_f32_e32 v94, v94, v95
	v_fmamk_f32 v94, v94, 0x3a800000, v191
	v_cmp_gt_f32_e32 vcc, s12, v94
	v_mul_f32_e32 v95, 0x4b800000, v94
	s_nop 0
	v_cndmask_b32_e32 v94, v94, v95, vcc
	v_rsq_f32_e32 v94, v94
	s_nop 0
	v_mul_f32_e32 v95, 0x45800000, v94
	v_cndmask_b32_e32 v94, v94, v95, vcc
	v_pk_mul_f32 v[0:1], v[0:1], v[94:95] op_sel_hi:[1,0]
	v_pk_mul_f32 v[2:3], v[2:3], v[94:95] op_sel_hi:[1,0]
	s_waitcnt vmcnt(0)
	v_pk_mul_f32 v[0:1], v[112:113], v[0:1]
	v_pk_mul_f32 v[2:3], v[114:115], v[2:3]
	v_cvt_pk_bf16_f32 v0, v0, v1
	v_cvt_pk_bf16_f32 v1, v2, v3
	v_pk_mul_f32 v[2:3], v[4:5], v[94:95] op_sel_hi:[1,0]
	v_pk_mul_f32 v[4:5], v[6:7], v[94:95] op_sel_hi:[1,0]
	v_pk_mul_f32 v[2:3], v[108:109], v[2:3]
	v_pk_mul_f32 v[4:5], v[110:111], v[4:5]
	v_cvt_pk_bf16_f32 v2, v2, v3
	v_cvt_pk_bf16_f32 v3, v4, v5
	v_pk_mul_f32 v[4:5], v[8:9], v[94:95] op_sel_hi:[1,0]
	v_pk_mul_f32 v[6:7], v[10:11], v[94:95] op_sel_hi:[1,0]
	v_pk_mul_f32 v[4:5], v[104:105], v[4:5]
	v_pk_mul_f32 v[6:7], v[6:7], v[106:107]
	v_cvt_pk_bf16_f32 v4, v4, v5
	v_cvt_pk_bf16_f32 v5, v6, v7
	v_pk_mul_f32 v[6:7], v[12:13], v[94:95] op_sel_hi:[1,0]
	v_pk_mul_f32 v[8:9], v[14:15], v[94:95] op_sel_hi:[1,0]
	v_pk_mul_f32 v[6:7], v[6:7], v[100:101]
	v_pk_mul_f32 v[8:9], v[8:9], v[102:103]
	v_cvt_pk_bf16_f32 v6, v6, v7
	v_cvt_pk_bf16_f32 v7, v8, v9
	global_store_dwordx4 v[74:75], v[0:3], off
	global_store_dwordx4 v[74:75], v[4:7], off offset:16
	s_nop 0
	v_mov_b32_e32 v0, v98
	s_andn2_b64 exec, exec, s[8:9]
	s_cbranch_execnz .LBB0_769
